# fp8 expert weights stored in a blocked layout (each 32-row x 128-k tile = one contiguous 4KB block): P0 writes 4KB contiguous per item, P7/P8 B-operand LDS-DMA addressing changed to match
# speedup vs baseline: 1.0024x; 1.0024x over previous
; __device__ __forceinline__ MoeItem moe_item(const float* wg, const float* wu, const float* wd, const float* win, const float* wout, const float* wpn, const float* wpd, unsigned char* ws, int r, int lane) {
;     ...
;     const int mat = r / MOE_IE, q = r % MOE_IE, e = mat / 3, which = mat % 3, kb = q / 64, nb = q % 64, n0 = nb * 32;
;     const float* src = (which == 0 ? wg : (which == 1 ? wu : wd)) + (size_t)e * DM * DFF + (size_t)(kb * 128 + (lane >> 5)) * DFF + n0 + (lane & 31);
;     unsigned char* dst;
;     if (which < 2) dst = ws + WS_WGUT + ((size_t)(e * 16 + (n0 >> 7)) * 256 + which * 128 + (n0 & 127)) * DM;
;     else dst = ws + WS_WDT + ((size_t)e * DM + n0) * DFF;
;     MoeItem it; it.stride = DFF; it.dpitch = DM; it.src = src; it.dst = dst + kb * 128 + (size_t)(lane >> 3) * DM + 16 * (lane & 7); return it;
;     ...
;         const int nmine = (NMOE - gw + NGW - 1) / NGW;
;         const int last = gw + (nmine - 1) * NGW;
;         MoeItem ia = moe_item(wg, wu, wd, win, wout, wpn, wpd, F.ws, gw, F.lane), ib = ia;
.LBB0_49:
	s_mov_b32 s32, 0
	s_abs_i32 s6, s72
	v_cvt_f32_u32_e32 v1, s6
	s_sub_i32 s4, s72, s3
	s_add_i32 s68, s4, 0x193ff
	s_sub_i32 s4, 0xfffe6c01, s4
	v_rcp_iflag_f32_e32 v1, v1
	s_max_i32 s7, s68, s4
	s_sub_i32 s4, 0, s6
	v_mul_f32_e32 v1, 0x4f7ffffe, v1
	v_cvt_u32_f32_e32 v1, v1
	s_nop 0
	v_readfirstlane_b32 s5, v1
	s_mul_i32 s4, s4, s5
	s_mul_hi_u32 s4, s5, s4
	s_add_i32 s5, s5, s4
	s_cmp_lt_i32 s3, 0x19000
	s_mul_hi_u32 s47, s7, s5
	s_cbranch_scc0 .LBB0_54
	s_cmp_lt_i32 s3, 0x18c00
	s_cbranch_scc0 .LBB0_56
	s_cmp_lt_i32 s3, 0x18000
	s_cbranch_scc0 .LBB0_57
	s_mov_b32 s32, 1
	s_ashr_i32 s4, s3, 31
	s_lshr_b32 s4, s4, 22
	s_add_i32 s4, s3, s4
	s_ashr_i32 s5, s4, 10
	s_and_b32 s4, s4, 0xfc00
	s_sub_i32 s38, s3, s4
	s_mul_hi_i32 s4, s3, 0x2aaaaaab
	s_lshr_b32 s39, s4, 31
	s_ashr_i32 s4, s4, 9
	s_add_i32 s4, s4, s39
	s_mul_hi_i32 s39, s5, 0x55555556
	s_lshr_b32 s42, s39, 31
	s_add_i32 s39, s39, s42
	s_mul_i32 s39, s39, 3
	s_sub_i32 s69, s5, s39
	s_sext_i32_i16 s5, s38
	s_bfe_u32 s5, s5, 0x60019
	s_add_i32 s42, s38, s5
	s_and_b32 s5, s42, 0xffc0
	s_sub_i32 s5, s38, s5
	s_sext_i32_i16 s70, s5
	s_lshl_b32 s38, s70, 5
	s_ashr_i32 s5, s4, 31
	s_ashr_i32 s39, s38, 31
	s_cmp_gt_i32 s69, 1
	s_sext_i32_i16 s71, s42
	s_cbranch_scc0 .LBB0_58
	s_lshl_b64 s[42:43], s[4:5], 22
	s_lshl_b64 s[44:45], s[38:39], 11
	s_add_u32 s42, s82, s42
	s_addc_u32 s43, s83, s43
	s_add_u32 s42, s42, s44
	s_addc_u32 s43, s43, s45
	s_add_u32 s42, s42, 0x24000000
	s_addc_u32 s43, s43, 0
	s_mov_b64 s[44:45], 0
	s_branch .LBB0_59

; __device__ __forceinline__ MoeItem moe_item(const float* wg, const float* wu, const float* wd, const float* win, const float* wout, const float* wpn, const float* wpd, unsigned char* ws, int r, int lane) {
;     ...
;     const int mat = r / MOE_IE, q = r % MOE_IE, e = mat / 3, which = mat % 3, kb = q / 64, nb = q % 64, n0 = nb * 32;
;     const float* src = (which == 0 ? wg : (which == 1 ? wu : wd)) + (size_t)e * DM * DFF + (size_t)(kb * 128 + (lane >> 5)) * DFF + n0 + (lane & 31);
;     unsigned char* dst;
;     if (which < 2) dst = ws + WS_WGUT + ((size_t)(e * 16 + (n0 >> 7)) * 256 + which * 128 + (n0 & 127)) * DM;
;     else dst = ws + WS_WDT + ((size_t)e * DM + n0) * DFF;
;     MoeItem it; it.stride = DFF; it.dpitch = DM; it.src = src; it.dst = dst + kb * 128 + (size_t)(lane >> 3) * DM + 16 * (lane & 7); return it;
.LBB0_55:
	s_mov_b64 s[38:39], 0x800
	s_mov_b64 s[42:43], 11
	s_cmp_eq_u32 s32, 1
	s_cselect_b32 s38, 0x80, s38
	s_cselect_b32 s42, 7, s42
	s_branch .LBB0_77

; __device__ __forceinline__ MoeItem moe_item(const float* wg, const float* wu, const float* wd, const float* win, const float* wout, const float* wpn, const float* wpd, unsigned char* ws, int r, int lane) {
;     ...
;     const int mat = r / MOE_IE, q = r % MOE_IE, e = mat / 3, which = mat % 3, kb = q / 64, nb = q % 64, n0 = nb * 32;
;     const float* src = (which == 0 ? wg : (which == 1 ? wu : wd)) + (size_t)e * DM * DFF + (size_t)(kb * 128 + (lane >> 5)) * DFF + n0 + (lane & 31);
;     unsigned char* dst;
;     if (which < 2) dst = ws + WS_WGUT + ((size_t)(e * 16 + (n0 >> 7)) * 256 + which * 128 + (n0 & 127)) * DM;
;     else dst = ws + WS_WDT + ((size_t)e * DM + n0) * DFF;
;     MoeItem it; it.stride = DFF; it.dpitch = DM; it.src = src; it.dst = dst + kb * 128 + (size_t)(lane >> 3) * DM + 16 * (lane & 7); return it;
.LBB0_61:
	s_cmp_eq_u32 s69, 1
	s_cselect_b32 s45, s20, s24
	s_cselect_b32 s70, s21, s25
	s_cmp_eq_u32 s69, 0
	s_cselect_b32 s69, s17, s70
	s_cselect_b32 s45, s16, s45
	s_lshl_b64 s[4:5], s[4:5], 24
	s_sext_i32_i16 s44, s44
	s_add_u32 s4, s45, s4
	s_addc_u32 s5, s69, s5
	s_lshl_b32 s44, s44, 7
	v_lshrrev_b32_e32 v1, 5, v170
	v_or_b32_e32 v4, s44, v1
	v_ashrrev_i32_e32 v5, 31, v4
	v_lshlrev_b64 v[4:5], 13, v[4:5]
	v_lshl_add_u64 v[4:5], s[4:5], 0, v[4:5]
	s_ashr_i32 s4, s44, 31
	v_lshl_add_u64 v[4:5], s[38:39], 2, v[4:5]
	v_and_b32_e32 v1, 31, v0
	s_lshl_b32 s98, s44, 5
	s_add_u32 s38, s42, s98
	v_lshlrev_b32_e32 v6, 2, v1
	v_mov_b32_e32 v7, 0
	s_addc_u32 s39, s43, s4
	v_lshl_add_u64 v[4:5], v[4:5], 0, v[6:7]
	v_mov_b64_e32 v[6:7], s[38:39]
	s_mov_b64 s[44:45], 0x800
	s_branch .LBB0_73

; #define MOE_LOAD(v, it) do { _Pragma("unroll") for (int i_ = 0; i_ < 64; ++i_) v[i_] = __builtin_nontemporal_load((it).src + (size_t)(2 * i_) * (it).stride); } while (0)
; __device__ __forceinline__ MoeItem moe_item(const float* wg, const float* wu, const float* wd, const float* win, const float* wout, const float* wpn, const float* wpd, unsigned char* ws, int r, int lane) {
;     ...
;     const int mat = r / MOE_IE, q = r % MOE_IE, e = mat / 3, which = mat % 3, kb = q / 64, nb = q % 64, n0 = nb * 32;
;     const float* src = (which == 0 ? wg : (which == 1 ? wu : wd)) + (size_t)e * DM * DFF + (size_t)(kb * 128 + (lane >> 5)) * DFF + n0 + (lane & 31);
;     unsigned char* dst;
;     if (which < 2) dst = ws + WS_WGUT + ((size_t)(e * 16 + (n0 >> 7)) * 256 + which * 128 + (n0 & 127)) * DM;
;     else dst = ws + WS_WDT + ((size_t)e * DM + n0) * DFF;
;     MoeItem it; it.stride = DFF; it.dpitch = DM; it.src = src; it.dst = dst + kb * 128 + (size_t)(lane >> 3) * DM + 16 * (lane & 7); return it;
;     ...
;             const int it1 = gw + (j + 1) * NGW, it2 = gw + (j + 2) * NGW;
;             ib = moe_item(wg, wu, wd, win, wout, wpn, wpd, F.ws, it1 <= last ? it1 : last, F.lane); MOE_LOAD(vb, ib);
.LBB0_81:
	s_mov_b32 s92, 0
	s_add_i32 s4, s72, s3
	s_min_i32 s70, s4, s7
	s_cmp_lt_i32 s70, 0x19000
	s_mov_b64 s[42:43], -1
	s_cbranch_scc0 .LBB0_102
	s_cmp_lt_i32 s70, 0x18c00
	s_cbranch_scc0 .LBB0_99
	s_cmp_lt_i32 s70, 0x18000
	s_cbranch_scc0 .LBB0_89
	s_mov_b32 s92, 1
	s_ashr_i32 s4, s70, 31
	s_lshr_b32 s4, s4, 22
	s_add_i32 s4, s70, s4
	s_ashr_i32 s43, s4, 10
	s_and_b32 s4, s4, 0xfc00
	s_sub_i32 s44, s70, s4
	s_mul_hi_i32 s4, s70, 0x2aaaaaab
	s_lshr_b32 s42, s4, 31
	s_ashr_i32 s4, s4, 9
	s_add_i32 s42, s4, s42
	s_mul_hi_i32 s4, s43, 0x55555556
	s_lshr_b32 s45, s4, 31
	s_add_i32 s4, s4, s45
	s_mul_i32 s4, s4, 3
	s_sub_i32 s4, s43, s4
	s_sext_i32_i16 s43, s44
	s_bfe_u32 s43, s43, 0x60019
	s_add_i32 s71, s44, s43
	s_and_b32 s43, s71, 0xffc0
	s_sub_i32 s43, s44, s43
	s_sext_i32_i16 s84, s43
	s_lshl_b32 s44, s84, 5
	s_ashr_i32 s43, s42, 31
	s_ashr_i32 s45, s44, 31
	s_cmp_gt_i32 s4, 1
	s_mov_b64 s[68:69], -1
	s_cbranch_scc0 .LBB0_86
	s_lshl_b64 s[46:47], s[42:43], 22
	s_lshl_b64 s[68:69], s[44:45], 11
	s_add_u32 s46, s73, s46
	s_addc_u32 s47, s74, s47
	s_add_u32 s46, s46, s68
	s_addc_u32 s47, s47, s69
	s_mov_b64 s[68:69], 0

; __device__ __forceinline__ MoeItem moe_item(const float* wg, const float* wu, const float* wd, const float* win, const float* wout, const float* wpn, const float* wpd, unsigned char* ws, int r, int lane) {
;     ...
;     const int mat = r / MOE_IE, q = r % MOE_IE, e = mat / 3, which = mat % 3, kb = q / 64, nb = q % 64, n0 = nb * 32;
;     const float* src = (which == 0 ? wg : (which == 1 ? wu : wd)) + (size_t)e * DM * DFF + (size_t)(kb * 128 + (lane >> 5)) * DFF + n0 + (lane & 31);
;     unsigned char* dst;
;     if (which < 2) dst = ws + WS_WGUT + ((size_t)(e * 16 + (n0 >> 7)) * 256 + which * 128 + (n0 & 127)) * DM;
;     else dst = ws + WS_WDT + ((size_t)e * DM + n0) * DFF;
;     MoeItem it; it.stride = DFF; it.dpitch = DM; it.src = src; it.dst = dst + kb * 128 + (size_t)(lane >> 3) * DM + 16 * (lane & 7); return it;
.LBB0_88:
	s_sext_i32_i16 s68, s71
	s_lshr_b32 s68, s68, 6
	s_cmp_eq_u32 s4, 1
	s_cselect_b32 s69, s20, s24
	s_cselect_b32 s71, s21, s25
	s_cmp_eq_u32 s4, 0
	s_cselect_b32 s4, s17, s71
	s_cselect_b32 s69, s16, s69
	s_lshl_b64 s[42:43], s[42:43], 24
	s_sext_i32_i16 s68, s68
	s_add_u32 s42, s69, s42
	s_addc_u32 s43, s4, s43
	s_lshl_b32 s4, s68, 7
	v_or_b32_e32 v12, s4, v20
	v_ashrrev_i32_e32 v13, 31, v12
	v_lshlrev_b64 v[12:13], 13, v[12:13]
	v_lshl_add_u64 v[12:13], s[42:43], 0, v[12:13]
	s_ashr_i32 s42, s4, 31
	v_lshl_add_u64 v[12:13], s[44:45], 2, v[12:13]
	s_lshl_b32 s98, s4, 5
	s_add_u32 s44, s46, s98
	v_lshlrev_b32_e32 v4, 2, v8
	s_addc_u32 s45, s47, s42
	v_lshl_add_u64 v[16:17], v[12:13], 0, v[4:5]
	s_mov_b64 s[42:43], 0
	v_mov_b64_e32 v[12:13], s[44:45]

; #define MOE_LOAD(v, it) do { _Pragma("unroll") for (int i_ = 0; i_ < 64; ++i_) v[i_] = __builtin_nontemporal_load((it).src + (size_t)(2 * i_) * (it).stride); } while (0)
;     ...
;             ib = moe_item(wg, wu, wd, win, wout, wpn, wpd, F.ws, it1 <= last ? it1 : last, F.lane); MOE_LOAD(vb, ib);
;             MOE_PROC(va, ia);
.LBB0_104:
	s_mov_b64 s[42:43], 0x800
	s_mov_b64 s[44:45], 11
	s_cmp_eq_u32 s92, 1
	s_cselect_b32 s42, 0x80, s42
	s_cselect_b32 s44, 7, s44
.LBB0_105:
	s_lshl_b64 s[46:47], s[46:47], 3
	global_load_dword v93, v[16:17], off nt
	v_lshl_add_u64 v[16:17], v[16:17], 0, s[46:47]
	v_lshl_add_u64 v[94:95], v[16:17], 0, s[46:47]
	v_lshl_add_u64 v[96:97], v[94:95], 0, s[46:47]
	v_lshl_add_u64 v[102:103], v[96:97], 0, s[46:47]
	v_lshl_add_u64 v[104:105], v[102:103], 0, s[46:47]
	v_lshl_add_u64 v[106:107], v[104:105], 0, s[46:47]
	v_lshl_add_u64 v[108:109], v[106:107], 0, s[46:47]
	v_lshl_add_u64 v[110:111], v[108:109], 0, s[46:47]
	global_load_dword v101, v[16:17], off nt
	global_load_dword v99, v[94:95], off nt
	global_load_dword v100, v[96:97], off nt
	s_nop 0
	global_load_dword v97, v[102:103], off nt
	global_load_dword v98, v[104:105], off nt
	global_load_dword v95, v[106:107], off nt
	global_load_dword v96, v[108:109], off nt
	global_load_dword v94, v[110:111], off nt
	v_lshl_add_u64 v[16:17], v[110:111], 0, s[46:47]
	s_waitcnt vmcnt(9)
	ds_write2st64_b32 v28, v87, v92 offset1:1
	v_lshl_add_u64 v[102:103], v[16:17], 0, s[46:47]
	global_load_dword v124, v[16:17], off nt
	global_load_dword v104, v[102:103], off nt
	v_lshl_add_u64 v[16:17], v[102:103], 0, s[46:47]
	global_load_dword v114, v[16:17], off nt
	v_lshl_add_u64 v[16:17], v[16:17], 0, s[46:47]
	global_load_dword v105, v[16:17], off nt
	v_lshl_add_u64 v[16:17], v[16:17], 0, s[46:47]
	global_load_dword v115, v[16:17], off nt
	v_lshl_add_u64 v[16:17], v[16:17], 0, s[46:47]
	global_load_dword v106, v[16:17], off nt
	v_lshl_add_u64 v[16:17], v[16:17], 0, s[46:47]
	global_load_dword v116, v[16:17], off nt
	v_lshl_add_u64 v[16:17], v[16:17], 0, s[46:47]
	global_load_dword v107, v[16:17], off nt
	v_lshl_add_u64 v[16:17], v[16:17], 0, s[46:47]
	global_load_dword v117, v[16:17], off nt
	v_lshl_add_u64 v[16:17], v[16:17], 0, s[46:47]
	global_load_dword v108, v[16:17], off nt
	v_lshl_add_u64 v[16:17], v[16:17], 0, s[46:47]
	global_load_dword v118, v[16:17], off nt
	v_lshl_add_u64 v[16:17], v[16:17], 0, s[46:47]
	global_load_dword v109, v[16:17], off nt
	v_lshl_add_u64 v[16:17], v[16:17], 0, s[46:47]
	global_load_dword v119, v[16:17], off nt
	v_lshl_add_u64 v[16:17], v[16:17], 0, s[46:47]
	global_load_dword v110, v[16:17], off nt
	v_lshl_add_u64 v[16:17], v[16:17], 0, s[46:47]
	global_load_dword v120, v[16:17], off nt
	v_lshl_add_u64 v[16:17], v[16:17], 0, s[46:47]
	global_load_dword v111, v[16:17], off nt
	v_lshl_add_u64 v[16:17], v[16:17], 0, s[46:47]
	global_load_dword v121, v[16:17], off nt
	v_lshl_add_u64 v[16:17], v[16:17], 0, s[46:47]
	global_load_dword v112, v[16:17], off nt
	v_lshl_add_u64 v[16:17], v[16:17], 0, s[46:47]
	global_load_dword v122, v[16:17], off nt
	v_lshl_add_u64 v[16:17], v[16:17], 0, s[46:47]
	global_load_dword v102, v[16:17], off nt
	v_lshl_add_u64 v[16:17], v[16:17], 0, s[46:47]
	global_load_dword v103, v[16:17], off nt
	v_lshl_add_u64 v[16:17], v[16:17], 0, s[46:47]
	global_load_dword v113, v[16:17], off nt
	v_lshl_add_u64 v[16:17], v[16:17], 0, s[46:47]
	global_load_dword v123, v[16:17], off nt
	v_lshl_add_u64 v[16:17], v[16:17], 0, s[46:47]
	global_load_dword v125, v[16:17], off nt
	v_lshl_add_u64 v[16:17], v[16:17], 0, s[46:47]
	global_load_dword v126, v[16:17], off nt
	v_lshl_add_u64 v[16:17], v[16:17], 0, s[46:47]
	global_load_dword v127, v[16:17], off nt
	v_lshl_add_u64 v[16:17], v[16:17], 0, s[46:47]
	global_load_dword v128, v[16:17], off nt
	v_lshl_add_u64 v[16:17], v[16:17], 0, s[46:47]
	global_load_dword v129, v[16:17], off nt
	v_lshl_add_u64 v[16:17], v[16:17], 0, s[46:47]
	global_load_dword v130, v[16:17], off nt
	v_lshl_add_u64 v[16:17], v[16:17], 0, s[46:47]
	global_load_dword v131, v[16:17], off nt
	v_lshl_add_u64 v[16:17], v[16:17], 0, s[46:47]
	global_load_dword v132, v[16:17], off nt
	v_lshl_add_u64 v[16:17], v[16:17], 0, s[46:47]
	global_load_dword v133, v[16:17], off nt
	v_lshl_add_u64 v[16:17], v[16:17], 0, s[46:47]
	global_load_dword v134, v[16:17], off nt
	v_lshl_add_u64 v[16:17], v[16:17], 0, s[46:47]
	global_load_dword v135, v[16:17], off nt
	v_lshl_add_u64 v[16:17], v[16:17], 0, s[46:47]
	global_load_dword v136, v[16:17], off nt
	v_lshl_add_u64 v[16:17], v[16:17], 0, s[46:47]
	global_load_dword v137, v[16:17], off nt
	v_lshl_add_u64 v[16:17], v[16:17], 0, s[46:47]
	global_load_dword v138, v[16:17], off nt
	v_lshl_add_u64 v[16:17], v[16:17], 0, s[46:47]
	global_load_dword v139, v[16:17], off nt
	v_lshl_add_u64 v[16:17], v[16:17], 0, s[46:47]
	global_load_dword v140, v[16:17], off nt
	v_lshl_add_u64 v[16:17], v[16:17], 0, s[46:47]
	global_load_dword v141, v[16:17], off nt
	v_lshl_add_u64 v[16:17], v[16:17], 0, s[46:47]
	global_load_dword v142, v[16:17], off nt
	v_lshl_add_u64 v[16:17], v[16:17], 0, s[46:47]
	global_load_dword v143, v[16:17], off nt
	v_lshl_add_u64 v[16:17], v[16:17], 0, s[46:47]
	global_load_dword v144, v[16:17], off nt
	v_lshl_add_u64 v[16:17], v[16:17], 0, s[46:47]
	global_load_dword v146, v[16:17], off nt
	v_lshl_add_u64 v[16:17], v[16:17], 0, s[46:47]
	global_load_dword v147, v[16:17], off nt
	v_lshl_add_u64 v[16:17], v[16:17], 0, s[46:47]
	global_load_dword v148, v[16:17], off nt
	v_lshl_add_u64 v[16:17], v[16:17], 0, s[46:47]
	global_load_dword v149, v[16:17], off nt
	v_lshl_add_u64 v[16:17], v[16:17], 0, s[46:47]
	global_load_dword v151, v[16:17], off nt
	v_lshl_add_u64 v[16:17], v[16:17], 0, s[46:47]
	global_load_dword v152, v[16:17], off nt
	v_lshl_add_u64 v[16:17], v[16:17], 0, s[46:47]
	global_load_dword v153, v[16:17], off nt
	v_lshl_add_u64 v[16:17], v[16:17], 0, s[46:47]
	global_load_dword v154, v[16:17], off nt
	v_lshl_add_u64 v[16:17], v[16:17], 0, s[46:47]
	global_load_dword v155, v[16:17], off nt
	v_lshl_add_u64 v[16:17], v[16:17], 0, s[46:47]
	global_load_dword v157, v[16:17], off nt
	v_lshl_add_u64 v[16:17], v[16:17], 0, s[46:47]
	global_load_dword v158, v[16:17], off nt
	v_lshl_add_u64 v[16:17], v[16:17], 0, s[46:47]
	ds_write2st64_b32 v28, v91, v90 offset0:2 offset1:3
	ds_write2st64_b32 v28, v89, v88 offset0:4 offset1:5
	ds_write2st64_b32 v28, v86, v85 offset0:6 offset1:7
	ds_write2st64_b32 v21, v83, v84 offset0:8 offset1:9
	ds_write2st64_b32 v21, v79, v80 offset0:10 offset1:11
	ds_write2st64_b32 v21, v75, v76 offset0:12 offset1:13
	ds_write2st64_b32 v21, v71, v72 offset0:14 offset1:15
	ds_write2st64_b32 v22, v65, v66 offset0:16 offset1:17
	ds_write2st64_b32 v22, v61, v62 offset0:18 offset1:19
	ds_write2st64_b32 v22, v57, v58 offset0:20 offset1:21
	ds_write2st64_b32 v22, v53, v54 offset0:22 offset1:23
	ds_write2st64_b32 v23, v45, v46 offset0:24 offset1:25
	ds_write2st64_b32 v23, v35, v36 offset0:26 offset1:27
	ds_write2st64_b32 v23, v33, v34 offset0:28 offset1:29
	ds_write2st64_b32 v23, v31, v32 offset0:30 offset1:31
	ds_write2st64_b32 v24, v29, v30 offset0:32 offset1:33
	ds_write2st64_b32 v24, v81, v82 offset0:34 offset1:35
	ds_write2st64_b32 v24, v77, v78 offset0:36 offset1:37
	ds_write2st64_b32 v24, v73, v74 offset0:38 offset1:39
	ds_write2st64_b32 v25, v69, v70 offset0:40 offset1:41
	ds_write2st64_b32 v25, v67, v68 offset0:42 offset1:43
	ds_write2st64_b32 v25, v63, v64 offset0:44 offset1:45
	ds_write2st64_b32 v25, v59, v60 offset0:46 offset1:47
	ds_write2st64_b32 v26, v55, v56 offset0:48 offset1:49
	ds_write2st64_b32 v26, v51, v52 offset0:50 offset1:51
	global_load_dword v159, v[16:17], off nt
	ds_write2st64_b32 v26, v38, v39 offset0:52 offset1:53
	ds_write2st64_b32 v26, v40, v42 offset0:54 offset1:55
	ds_write2st64_b32 v27, v37, v41 offset0:56 offset1:57
	ds_write2st64_b32 v27, v43, v44 offset0:58 offset1:59
	ds_write2st64_b32 v27, v47, v48 offset0:60 offset1:61
	ds_write2st64_b32 v27, v49, v50 offset0:62 offset1:63
	s_waitcnt lgkmcnt(0)
	ds_read2_b32 v[16:17], v1 offset1:32
	v_mov_b32_e32 v30, 0
	ds_read2_b32 v[32:33], v1 offset0:128 offset1:160
	v_mov_b32_e32 v31, 0
	v_add_u32_e32 v145, 0x400, v1
	s_waitcnt lgkmcnt(1)
	v_mul_f32_e32 v4, 0x42800000, v16
	v_mul_f32_e32 v15, 0x42800000, v17
	ds_read2_b32 v[16:17], v1 offset0:64 offset1:96
	v_cvt_pk_fp8_f32 v30, v4, v15
	ds_read2_b32 v[34:35], v145 offset0:128 offset1:160
	v_add_u32_e32 v150, 0x400, v9
	ds_read2_b32 v[38:39], v150 offset0:128 offset1:160
	s_waitcnt lgkmcnt(2)
	v_mul_f32_e32 v4, 0x42800000, v16
	v_mul_f32_e32 v15, 0x42800000, v17
	ds_read2_b32 v[16:17], v1 offset0:192 offset1:224
	v_cvt_pk_fp8_f32 v30, v4, v15 op_sel:[0,0,1]
	v_mul_f32_e32 v4, 0x42800000, v32
	v_mul_f32_e32 v15, 0x42800000, v33
	v_cvt_pk_fp8_f32 v31, v4, v15
	s_waitcnt lgkmcnt(0)
	v_mul_f32_e32 v4, 0x42800000, v16
	v_mul_f32_e32 v15, 0x42800000, v17
	ds_read2_b32 v[16:17], v145 offset0:64 offset1:96
	ds_read2_b32 v[32:33], v145 offset1:32
	v_cvt_pk_fp8_f32 v31, v4, v15 op_sel:[0,0,1]
	v_lshl_add_u64 v[10:11], v[10:11], 0, v[6:7]
	v_add_u32_e32 v156, 0x400, v18
	s_waitcnt lgkmcnt(1)
	v_mul_f32_e32 v29, 0x42800000, v16
	v_mul_f32_e32 v36, 0x42800000, v17
	ds_read2_b32 v[16:17], v145 offset0:192 offset1:224
	s_waitcnt lgkmcnt(1)
	v_mul_f32_e32 v4, 0x42800000, v32
	v_mul_f32_e32 v15, 0x42800000, v33
	v_mov_b32_e32 v32, 0
	v_cvt_pk_fp8_f32 v32, v4, v15
	v_mul_f32_e32 v4, 0x42800000, v34
	v_mul_f32_e32 v15, 0x42800000, v35
	v_mov_b32_e32 v33, 0
	ds_read2_b32 v[34:35], v9 offset1:32
	v_cvt_pk_fp8_f32 v33, v4, v15
	s_waitcnt lgkmcnt(1)
	v_mul_f32_e32 v4, 0x42800000, v16
	v_mul_f32_e32 v15, 0x42800000, v17
	ds_read2_b32 v[16:17], v9 offset0:64 offset1:96
	v_cvt_pk_fp8_f32 v32, v29, v36 op_sel:[0,0,1]
	ds_read2_b32 v[36:37], v9 offset0:128 offset1:160
	v_cvt_pk_fp8_f32 v33, v4, v15 op_sel:[0,0,1]
	s_waitcnt lgkmcnt(2)
	v_mul_f32_e32 v4, 0x42800000, v34
	v_mul_f32_e32 v15, 0x42800000, v35
	v_mov_b32_e32 v34, 0
	v_cvt_pk_fp8_f32 v34, v4, v15
	s_waitcnt lgkmcnt(1)
	v_mul_f32_e32 v4, 0x42800000, v16
	v_mul_f32_e32 v15, 0x42800000, v17
	ds_read2_b32 v[16:17], v9 offset0:192 offset1:224
	s_waitcnt lgkmcnt(1)
	v_mul_f32_e32 v29, 0x42800000, v36
	v_mul_f32_e32 v36, 0x42800000, v37
	v_mov_b32_e32 v35, 0
	v_cvt_pk_fp8_f32 v35, v29, v36
	ds_read2_b32 v[36:37], v150 offset1:32
	v_cvt_pk_fp8_f32 v34, v4, v15 op_sel:[0,0,1]
	s_waitcnt lgkmcnt(1)
	v_mul_f32_e32 v4, 0x42800000, v16
	v_mul_f32_e32 v15, 0x42800000, v17
	ds_read2_b32 v[16:17], v150 offset0:64 offset1:96
	v_cvt_pk_fp8_f32 v35, v4, v15 op_sel:[0,0,1]
	s_waitcnt lgkmcnt(1)
	v_mul_f32_e32 v4, 0x42800000, v36
	v_mul_f32_e32 v15, 0x42800000, v37
	v_mov_b32_e32 v36, 0
	v_cvt_pk_fp8_f32 v36, v4, v15
	s_waitcnt lgkmcnt(0)
; __device__ __forceinline__ MoeItem moe_item(const float* wg, const float* wu, const float* wd, const float* win, const float* wout, const float* wpn, const float* wpd, unsigned char* ws, int r, int lane) {
;     ...
;     const int mat = r / MOE_IE, q = r % MOE_IE, e = mat / 3, which = mat % 3, kb = q / 64, nb = q % 64, n0 = nb * 32;
;     const float* src = (which == 0 ? wg : (which == 1 ? wu : wd)) + (size_t)e * DM * DFF + (size_t)(kb * 128 + (lane >> 5)) * DFF + n0 + (lane & 31);
;     unsigned char* dst;
;     if (which < 2) dst = ws + WS_WGUT + ((size_t)(e * 16 + (n0 >> 7)) * 256 + which * 128 + (n0 & 127)) * DM;
;     else dst = ws + WS_WDT + ((size_t)e * DM + n0) * DFF;
;     MoeItem it; it.stride = DFF; it.dpitch = DM; it.src = src; it.dst = dst + kb * 128 + (size_t)(lane >> 3) * DM + 16 * (lane & 7); return it;
	v_mul_f32_e32 v4, 0x42800000, v16
	v_mul_f32_e32 v15, 0x42800000, v17
	ds_read2_b32 v[16:17], v150 offset0:192 offset1:224
	v_cvt_pk_fp8_f32 v36, v4, v15 op_sel:[0,0,1]
	v_mul_f32_e32 v4, 0x42800000, v38
	v_mul_f32_e32 v15, 0x42800000, v39
	v_mov_b32_e32 v37, 0
	v_cvt_pk_fp8_f32 v37, v4, v15
	s_waitcnt lgkmcnt(0)
	v_mul_f32_e32 v4, 0x42800000, v16
	v_mul_f32_e32 v15, 0x42800000, v17
	ds_read2_b32 v[16:17], v18 offset1:32
	v_cvt_pk_fp8_f32 v37, v4, v15 op_sel:[0,0,1]
	global_store_dwordx4 v[10:11], v[30:33], off
	ds_read2_b32 v[32:33], v18 offset0:64 offset1:96
	s_lshl_b64 s[38:39], s[38:39], 3
	s_waitcnt lgkmcnt(1)
	v_mul_f32_e32 v4, 0x42800000, v16
	v_mul_f32_e32 v15, 0x42800000, v17
	ds_read2_b32 v[16:17], v18 offset0:128 offset1:160
	v_mov_b32_e32 v30, 0
	v_cvt_pk_fp8_f32 v30, v4, v15
	s_waitcnt lgkmcnt(1)
	v_mul_f32_e32 v4, 0x42800000, v32
	v_mov_b32_e32 v31, 0
	s_waitcnt lgkmcnt(0)
	v_mul_f32_e32 v29, 0x42800000, v16
	v_mul_f32_e32 v32, 0x42800000, v17
	ds_read2_b32 v[16:17], v18 offset0:192 offset1:224
	v_mul_f32_e32 v15, 0x42800000, v33
	v_cvt_pk_fp8_f32 v31, v29, v32
	ds_read2_b32 v[32:33], v156 offset1:32
	v_cvt_pk_fp8_f32 v30, v4, v15 op_sel:[0,0,1]
	s_waitcnt lgkmcnt(1)
	v_mul_f32_e32 v4, 0x42800000, v16
	v_mul_f32_e32 v15, 0x42800000, v17
	ds_read2_b32 v[16:17], v156 offset0:64 offset1:96
	v_lshl_add_u64 v[10:11], v[10:11], 0, s[38:39]
	global_store_dwordx4 v[10:11], v[34:37], off
	ds_read2_b32 v[34:35], v156 offset0:128 offset1:160
	v_cvt_pk_fp8_f32 v31, v4, v15 op_sel:[0,0,1]
	s_waitcnt lgkmcnt(2)
	v_mul_f32_e32 v4, 0x42800000, v32
	v_mul_f32_e32 v15, 0x42800000, v33
	v_mov_b32_e32 v32, 0
	v_cvt_pk_fp8_f32 v32, v4, v15
	s_waitcnt lgkmcnt(1)
	v_mul_f32_e32 v4, 0x42800000, v16
	v_mul_f32_e32 v15, 0x42800000, v17
	ds_read2_b32 v[16:17], v156 offset0:192 offset1:224
	s_waitcnt lgkmcnt(1)
	v_mul_f32_e32 v29, 0x42800000, v34
	v_mul_f32_e32 v34, 0x42800000, v35
	v_mov_b32_e32 v33, 0
	v_cvt_pk_fp8_f32 v33, v29, v34
	ds_read2_b32 v[34:35], v19 offset1:32
	v_cvt_pk_fp8_f32 v32, v4, v15 op_sel:[0,0,1]
	s_waitcnt lgkmcnt(1)
	v_mul_f32_e32 v4, 0x42800000, v16
	v_mul_f32_e32 v15, 0x42800000, v17
	ds_read2_b32 v[16:17], v19 offset0:64 offset1:96
	ds_read2_b32 v[36:37], v19 offset0:128 offset1:160
	v_cvt_pk_fp8_f32 v33, v4, v15 op_sel:[0,0,1]
	s_waitcnt lgkmcnt(2)
	v_mul_f32_e32 v4, 0x42800000, v34
	v_mul_f32_e32 v15, 0x42800000, v35
	v_mov_b32_e32 v34, 0
	v_cvt_pk_fp8_f32 v34, v4, v15
	s_waitcnt lgkmcnt(1)
	v_mul_f32_e32 v4, 0x42800000, v16
	v_mul_f32_e32 v15, 0x42800000, v17
	ds_read2_b32 v[16:17], v19 offset0:192 offset1:224
	s_waitcnt lgkmcnt(1)
	v_mul_f32_e32 v29, 0x42800000, v36
	v_mul_f32_e32 v36, 0x42800000, v37
	v_mov_b32_e32 v35, 0
	v_add_u32_e32 v160, 0x400, v19
	v_cvt_pk_fp8_f32 v35, v29, v36
	ds_read2_b32 v[36:37], v160 offset1:32
	v_cvt_pk_fp8_f32 v34, v4, v15 op_sel:[0,0,1]
	s_waitcnt lgkmcnt(1)
	v_mul_f32_e32 v4, 0x42800000, v16
	v_mul_f32_e32 v15, 0x42800000, v17
	ds_read2_b32 v[16:17], v160 offset0:64 offset1:96
	ds_read2_b32 v[38:39], v160 offset0:128 offset1:160
	v_cvt_pk_fp8_f32 v35, v4, v15 op_sel:[0,0,1]
	s_waitcnt lgkmcnt(2)
	v_mul_f32_e32 v4, 0x42800000, v36
	v_mul_f32_e32 v15, 0x42800000, v37
	v_mov_b32_e32 v36, 0
	v_cvt_pk_fp8_f32 v36, v4, v15
	s_waitcnt lgkmcnt(1)
	v_mul_f32_e32 v4, 0x42800000, v16
	v_mul_f32_e32 v15, 0x42800000, v17
	ds_read2_b32 v[16:17], v160 offset0:192 offset1:224
	s_waitcnt lgkmcnt(1)
	v_mul_f32_e32 v29, 0x42800000, v38
	v_mul_f32_e32 v38, 0x42800000, v39
	v_mov_b32_e32 v37, 0
	v_cvt_pk_fp8_f32 v37, v29, v38
	v_cvt_pk_fp8_f32 v36, v4, v15 op_sel:[0,0,1]
	s_waitcnt lgkmcnt(0)
	v_mul_f32_e32 v4, 0x42800000, v16
	v_mul_f32_e32 v15, 0x42800000, v17
	v_cvt_pk_fp8_f32 v37, v4, v15 op_sel:[0,0,1]
	v_lshl_add_u64 v[10:11], v[10:11], 0, s[38:39]
	global_store_dwordx4 v[10:11], v[30:33], off
	v_lshl_add_u64 v[10:11], v[10:11], 0, s[38:39]
	global_store_dwordx4 v[10:11], v[34:37], off
	s_waitcnt lgkmcnt(0)
	s_add_i32 s3, s89, s3
	s_mov_b32 s96, 0
	s_min_i32 s43, s3, s7
	s_cmp_lt_i32 s43, 0x19000
	s_mov_b64 s[38:39], -1
	s_cbranch_scc0 .LBB0_126
	s_cmp_lt_i32 s43, 0x18c00
	s_cbranch_scc0 .LBB0_123
	s_cmp_lt_i32 s43, 0x18000
	s_cbranch_scc0 .LBB0_113
	s_mov_b32 s96, 1
	s_ashr_i32 s4, s43, 31
	s_lshr_b32 s4, s4, 22
	s_add_i32 s4, s43, s4
	s_ashr_i32 s39, s4, 10
	s_and_b32 s4, s4, 0xfc00
	s_sub_i32 s46, s43, s4
	s_mul_hi_i32 s4, s43, 0x2aaaaaab
	s_lshr_b32 s38, s4, 31
	s_ashr_i32 s4, s4, 9
	s_add_i32 s38, s4, s38
	s_mul_hi_i32 s4, s39, 0x55555556
	s_lshr_b32 s45, s4, 31
	s_add_i32 s4, s4, s45
	s_mul_i32 s4, s4, 3
	s_sub_i32 s4, s39, s4
	s_sext_i32_i16 s39, s46
	s_bfe_u32 s39, s39, 0x60019
	s_add_i32 s45, s46, s39
	s_and_b32 s39, s45, 0xffc0
	s_sub_i32 s39, s46, s39
	s_sext_i32_i16 s84, s39
	s_lshl_b32 s46, s84, 5
	s_ashr_i32 s39, s38, 31
	s_ashr_i32 s47, s46, 31
	s_cmp_gt_i32 s4, 1
	s_mov_b64 s[70:71], -1
	s_cbranch_scc0 .LBB0_110
	s_lshl_b64 s[68:69], s[38:39], 22
	s_lshl_b64 s[70:71], s[46:47], 11
	s_add_u32 s68, s73, s68
	s_addc_u32 s69, s74, s69
	s_add_u32 s68, s68, s70
	s_addc_u32 s69, s69, s71
	s_mov_b64 s[70:71], 0

; __device__ __forceinline__ MoeItem moe_item(const float* wg, const float* wu, const float* wd, const float* win, const float* wout, const float* wpn, const float* wpd, unsigned char* ws, int r, int lane) {
;     ...
;     const int mat = r / MOE_IE, q = r % MOE_IE, e = mat / 3, which = mat % 3, kb = q / 64, nb = q % 64, n0 = nb * 32;
;     const float* src = (which == 0 ? wg : (which == 1 ? wu : wd)) + (size_t)e * DM * DFF + (size_t)(kb * 128 + (lane >> 5)) * DFF + n0 + (lane & 31);
;     unsigned char* dst;
;     if (which < 2) dst = ws + WS_WGUT + ((size_t)(e * 16 + (n0 >> 7)) * 256 + which * 128 + (n0 & 127)) * DM;
;     else dst = ws + WS_WDT + ((size_t)e * DM + n0) * DFF;
;     MoeItem it; it.stride = DFF; it.dpitch = DM; it.src = src; it.dst = dst + kb * 128 + (size_t)(lane >> 3) * DM + 16 * (lane & 7); return it;
.LBB0_112:
	s_sext_i32_i16 s45, s45
	s_lshr_b32 s45, s45, 6
	s_cmp_eq_u32 s4, 1
	s_cselect_b32 s70, s20, s24
	s_cselect_b32 s71, s21, s25
	s_cmp_eq_u32 s4, 0
	s_cselect_b32 s4, s17, s71
	s_cselect_b32 s70, s16, s70
	s_lshl_b64 s[38:39], s[38:39], 24
	s_sext_i32_i16 s45, s45
	s_add_u32 s38, s70, s38
	s_addc_u32 s39, s4, s39
	s_lshl_b32 s4, s45, 7
	v_or_b32_e32 v10, s4, v20
	v_ashrrev_i32_e32 v11, 31, v10
	v_lshlrev_b64 v[10:11], 13, v[10:11]
	v_lshl_add_u64 v[10:11], s[38:39], 0, v[10:11]
	s_ashr_i32 s38, s4, 31
	v_lshl_add_u64 v[10:11], s[46:47], 2, v[10:11]
	s_lshl_b32 s98, s4, 5
	s_add_u32 s46, s68, s98
	v_mov_b32_e32 v15, v5
	s_addc_u32 s47, s69, s38
	v_lshl_add_u64 v[16:17], v[10:11], 0, v[14:15]
	s_mov_b64 s[38:39], 0
	v_mov_b64_e32 v[10:11], s[46:47]

; __device__ __forceinline__ MoeItem moe_item(const float* wg, const float* wu, const float* wd, const float* win, const float* wout, const float* wpn, const float* wpd, unsigned char* ws, int r, int lane) {
;     if (r >= NMOE_X + NGATE_IT + NWO_IT) { const int q = r - NMOE_X - NGATE_IT - NWO_IT, which = q >> 9, kb = (q >> 6) & 7, nb = q & 63; MoeItem it; it.stride = DM; it.dpitch = 1024;
;         it.src = (which ? wpd : wpn) + (size_t)(kb * 128 + (lane >> 5)) * DM + nb * 32 + (lane & 31);
;         it.dst = ws + (which ? WS_WPDFT : WS_WPNAT) + (size_t)(nb * 32) * 1024 + kb * 128 + (size_t)(lane >> 3) * 1024 + 16 * (lane & 7); return it; }
;     if (r >= NMOE_X + NGATE_IT) { const int q = r - NMOE_X - NGATE_IT, kb = q >> 6, nb = q & 63; MoeItem it; it.stride = DM; it.dpitch = DM;
;         it.src = wout + (size_t)(kb * 128 + (lane >> 5)) * DM + nb * 32 + (lane & 31);
;         it.dst = ws + WS_WO8 + (size_t)(nb * 32) * DM + kb * 128 + (size_t)(lane >> 3) * DM + 16 * (lane & 7); return it; }
;     if (r >= NMOE_X) { const int q = r - NMOE_X, kb = q / 192, nb = q % 192; MoeItem it; it.stride = INC; it.dpitch = DM;
;         const int scol = nb < 128 ? 6144 + nb * 32 : (nb < 160 ? 1024 + (nb - 128) * 32 : 3072 + (nb - 160) * 32);
;         it.src = win + (size_t)(kb * 128 + (lane >> 5)) * INC + scol + (lane & 31);
;         it.dst = ws + WS_WG8 + (size_t)(nb * 32) * DM + kb * 128 + (size_t)(lane >> 3) * DM + 16 * (lane & 7); return it; }
;     const int mat = r / MOE_IE, q = r % MOE_IE, e = mat / 3, which = mat % 3, kb = q / 64, nb = q % 64, n0 = nb * 32;
;     const float* src = (which == 0 ? wg : (which == 1 ? wu : wd)) + (size_t)e * DM * DFF + (size_t)(kb * 128 + (lane >> 5)) * DFF + n0 + (lane & 31);
;     unsigned char* dst;
;     if (which < 2) dst = ws + WS_WGUT + ((size_t)(e * 16 + (n0 >> 7)) * 256 + which * 128 + (n0 & 127)) * DM;
;     else dst = ws + WS_WDT + ((size_t)e * DM + n0) * DFF;
;     MoeItem it; it.stride = DFF; it.dpitch = DM; it.src = src; it.dst = dst + kb * 128 + (size_t)(lane >> 3) * DM + 16 * (lane & 7); return it;
.LBB0_126:
	s_andn2_b64 vcc, exec, s[38:39]
	s_cbranch_vccz .LBB0_79
	s_mov_b64 s[38:39], 0x800
	s_mov_b64 s[46:47], 11
	s_cmp_eq_u32 s96, 1
	s_cselect_b32 s38, 0x80, s38
	s_cselect_b32 s46, 7, s46
	s_branch .LBB0_80

; template <class Epi, class Sched, bool GATHER, bool F8 = false>
; __device__ __forceinline__ void gemm_phase(LAS unsigned char* lds, const int K, const Sched& S, const Epi& E) {
;     ...
;     for (int i = 0; i < 2; ++i) { int R, C; stage_rc(tid * 16 + i * 8192, R, C); const int Rb = epi_wide<Epi>() ? (64 * (R >> 5) + perm32(R & 31)) : (Epi::PERM ? ((R & ~31) + perm32(R & 31)) : R);
;         RA[i] = R; CA[i] = C; voffB[i] = (unsigned)(Rb * K + C) * 2u;
;         vA[0][i] = (unsigned)(R * K + C) * 2u; vA[1][i] = vA[0][i] + (unsigned)hstep; }
;     const unsigned ldsw = (unsigned)wid * 1024u;
;     const int aoff = lds_byte(wr * 64 + fr, fq * 8), boff = lds_byte(wc * 32 + fr, fq * 8);
;     ...
;     Unit cur, nxt; int ui = 0;
;     if (!S.next(0, cur)) return;
;     if constexpr (GATHER) { S.offsets(0, RA, CA, vA); }
; #pragma unroll
;     for (int h = 0; h < 2; ++h)
; #pragma unroll
;         for (int i = 0; i < 2; ++i) vN[h][i] = vA[h][i];
;     f32x4 acc[2][2][4][2];
; #pragma unroll
;     for (int a = 0; a < 2; ++a)
; #pragma unroll
;         for (int b = 0; b < 2; ++b)
; #pragma unroll
;             for (int m = 0; m < 4; ++m)
; #pragma unroll
;                 for (int n = 0; n < 2; ++n) acc[a][b][m][n] = (f32x4){0.f, 0.f, 0.f, 0.f};
;     if constexpr (EpiInit<Epi>::value) { const typename EpiInit<Epi>::Pre p0 = E.preload(cur, wr, wc, fr, fq); E.init(acc, p0); }
;     int one_scale = 0x7f7f7f7f; asm volatile("" : "+v"(one_scale));
;     bf16x8 At[4][2], B0[2][2], B1[2][2]; i32x8 At8[4], B08[2], B18[2];
;     const char* cA = cur.A; const char* cB = cur.B;
;     PG8_STAGE(PG8_SB(0, 0), cB, voffB); PG8_STAGE(PG8_SB(0, 1), cB + hstepB, voffB); PG8_STAGE(PG8_SA(0, 0), cA, vA[0]); PG8_STAGE(PG8_SA(0, 1), cA, vA[1]);
;     if (wr == 1) PG8_BAR;
; __global__ void __launch_bounds__(512, 2) fwd(Args args) {
;     ...
;         { LAS int* tab = (LAS int*)(F.lds + TAB_OFF); const int* tokl = (const int*)(F.ws + WS_TOKL);
;           const int r = F.tid & 255, ih = F.tid >> 8; int toks[5];
; #pragma unroll
;           for (int k = 0; k < 5; ++k) { Unit u; toks[k] = 0;
;               if (S.next(2 * k + ih, u)) { const int tile = u.row0 >> 8, e = u.tag, r0 = tab[160 + tile] * 256, n = tab[320 + e]; if (r0 + r < n) toks[k] = tokl[e * NTOK + r0 + r]; } }
; #pragma unroll
;           for (int k = 0; k < 5; ++k) tab[512 + (2 * k + ih) * 256 + r] = toks[k];
;           __syncthreads(); }
.LBB0_1027:
	s_or_b64 exec, exec, s[10:11]
	v_and_b32_e32 v2, 0x100, v0
	v_mov_b32_e32 v5, 2
	s_add_i32 s0, 0, 0x20000
	v_lshlrev_b32_e32 v2, 2, v2
	v_lshlrev_b32_sdwa v5, v5, v0 dst_sel:DWORD dst_unused:UNUSED_PAD src0_sel:DWORD src1_sel:BYTE_0
	s_or_b32 s6, s6, s7
	v_add3_u32 v2, s0, v2, v5
	s_cmp_ge_i32 s6, s3
	v_readfirstlane_b32 s20, v0
	s_waitcnt vmcnt(0)
	ds_write2st64_b32 v2, v4, v1 offset0:8 offset1:16
	ds_write2st64_b32 v2, v7, v6 offset0:24 offset1:32
	ds_write_b32 v2, v3 offset:10240
	s_waitcnt lgkmcnt(0)
	s_barrier
	s_cbranch_scc1 .LBB0_1045
	v_lshlrev_b32_e32 v1, 4, v0
	v_and_b32_e32 v2, 32, v0
	v_bfe_u32 v4, v0, 3, 25
	s_add_u32 s7, s82, 0x4000000
	v_bfe_u32 v3, v0, 2, 4
	v_bitop3_b32 v1, v1, v2, 48 bitop3:0x6c
	v_lshrrev_b32_e32 v2, 3, v0
	v_or_b32_e32 v4, 64, v4
	s_movk_i32 s0, 0x70
	s_addc_u32 s25, s83, 0
	v_and_or_b32 v160, v2, 48, v3
	v_and_or_b32 v161, v4, s0, v3
	s_lshl_b32 s0, s20, 4
	v_lshrrev_b32_e32 v3, 1, v0
	s_and_b32 s37, s0, 0xfffffc00
	v_and_b32_e32 v14, 24, v3
	s_lshr_b32 s0, s20, 1
	v_lshrrev_b32_e32 v3, 5, v0
	s_lshr_b32 s21, s20, 8
	s_and_b32 s14, s0, 0x60
	v_and_b32_e32 v3, 4, v3
	v_bfe_u32 v5, v0, 2, 2
	s_movk_i32 s10, 0x60
	s_add_u32 s0, s82, 0x2c000000
	v_or3_b32 v3, v3, v5, v14
	s_addc_u32 s1, s83, 0
	v_and_or_b32 v4, v4, s10, v3
	s_lshl_b32 s10, s6, 2
	s_add_i32 s10, s10, 0
	v_and_or_b32 v1, v0, 64, v1
	v_and_or_b32 v2, v2, 32, v3
	s_add_i32 s10, s10, 0x20000
	v_lshl_or_b32 v148, v2, 11, v1
	v_mov_b32_e32 v2, s10
	ds_read_b32 v150, v2
	s_lshl_b32 s10, s2, 3
	s_and_b32 s39, s10, 8
	s_ashr_i32 s10, s2, 5
	s_add_i32 s39, s39, s10
	s_waitcnt lgkmcnt(0)
	v_readfirstlane_b32 s10, v150
	s_lshl_b32 s10, s10, 4
	s_add_i32 s10, s10, s39
	s_ashr_i32 s11, s10, 31
	s_lshl_b64 s[10:11], s[10:11], 19
	s_add_u32 s44, s7, s10
	v_lshl_or_b32 v146, v4, 11, v1
	v_bfe_u32 v254, v148, 11, 5
	v_and_b32_e32 v148, 0xffff007f, v148
	v_lshl_or_b32 v148, v254, 7, v148
	v_bfe_u32 v254, v146, 11, 5
	v_and_b32_e32 v146, 0xffff007f, v146
	v_lshl_or_b32 v146, v254, 7, v146
	s_addc_u32 s45, s25, s11
	s_add_i32 s10, 0, 0x20800
	v_lshlrev_b32_e32 v2, 2, v160
	v_lshlrev_b32_e32 v4, 2, v161
	v_add_u32_e32 v3, s10, v2
	v_add_u32_e32 v5, s10, v4
	s_add_i32 s10, 0, 0x20a00
	v_add_u32_e32 v2, s10, v2
	v_add_u32_e32 v4, s10, v4
	ds_read_b32 v3, v3
	ds_read_b32 v5, v5
	ds_read_b32 v2, v2
	ds_read_b32 v4, v4
	s_lshl_b32 s50, s39, 7
	v_or_b32_e32 v162, s14, v14
	v_ashrrev_i32_e32 v151, 31, v150
	s_waitcnt lgkmcnt(1)
	v_lshl_or_b32 v163, v2, 11, v1
	v_or_b32_e32 v2, s50, v162
	v_lshl_or_b32 v152, v3, 11, v1
	v_lshl_or_b32 v154, v5, 11, v1
	s_waitcnt lgkmcnt(0)
	v_lshl_or_b32 v164, v4, 11, v1
	v_lshlrev_b64 v[4:5], 13, v[150:151]
	v_ashrrev_i32_e32 v3, 31, v2
	v_lshl_add_u64 v[6:7], s[18:19], 0, v[4:5]
	v_lshlrev_b64 v[2:3], 2, v[2:3]
	s_add_i32 s51, s37, 0
	v_lshl_add_u64 v[10:11], v[6:7], 0, v[2:3]
	v_lshl_add_u64 v[4:5], s[22:23], 0, v[4:5]
	v_mov_b32_e32 v165, 0x7f7f7f7f
	s_add_i32 m0, s51, 0x10000
	v_lshl_add_u64 v[12:13], v[4:5], 0, v[2:3]
	global_load_dwordx4 v[58:61], v[10:11], off offset:16
	global_load_dwordx4 v[62:65], v[10:11], off
	global_load_dwordx4 v[2:5], v[12:13], off offset:16
	global_load_dwordx4 v[6:9], v[12:13], off
	global_load_lds_dwordx4 v148, s[44:45]
	s_add_i32 m0, s51, 0x12000
	s_add_u32 s10, s44, 0x40000
	global_load_lds_dwordx4 v146, s[44:45]
	s_addc_u32 s11, s45, 0
	s_add_i32 m0, s51, 0x14000
	s_add_i32 s52, s51, 0x2000
	global_load_lds_dwordx4 v148, s[10:11]
	s_add_i32 m0, s51, 0x16000
	s_add_i32 s53, s51, 0x4000
	global_load_lds_dwordx4 v146, s[10:11]
	s_mov_b32 m0, s51
	s_add_i32 s54, s51, 0x6000
	global_load_lds_dwordx4 v152, s[0:1]
	s_mov_b32 m0, s52
	v_mov_b32_e32 v153, 0
	global_load_lds_dwordx4 v154, s[0:1]
	s_mov_b32 m0, s53
	v_mov_b32_e32 v149, v153
	global_load_lds_dwordx4 v163, s[0:1]
	s_mov_b32 m0, s54
	v_mov_b32_e32 v147, v153
	global_load_lds_dwordx4 v164, s[0:1]
	s_cmp_eq_u32 s21, 1
	v_lshl_add_u64 v[12:13], s[44:45], 0, v[148:149]
	v_lshl_add_u64 v[10:11], s[44:45], 0, v[146:147]
	s_cselect_b64 s[10:11], -1, 0
	s_cmp_lg_u32 s21, 1
	v_mov_b32_e32 v155, v153
	s_cbranch_scc1 .LBB0_1030
	s_barrier
.LBB0_1030:
	s_lshl_b32 s64, s6, 8
	s_add_u32 s12, s82, 0x34000000
	s_addc_u32 s13, s83, 0
	s_lshl_b32 s36, s14, 7
	s_mov_b64 s[14:15], 0x80
	s_mov_b64 s[100:101], 0x1000
	s_add_i32 m0, s51, 0x18000
	v_lshl_add_u64 v[12:13], v[12:13], 0, s[100:101]
	s_lshl_b32 s24, s21, 13
	s_waitcnt vmcnt(2)
	s_barrier
	global_load_lds_dwordx4 v[12:13], off
	s_add_i32 m0, s51, 0x1a000
	s_add_u32 s16, s82, 0x2c000080
	v_lshl_add_u64 v[10:11], v[10:11], 0, s[100:101]
	s_addc_u32 s17, s83, 0
	s_add_i32 s55, s51, 0x8000
	s_add_i32 s56, s51, 0xa000
	global_load_lds_dwordx4 v[10:11], off
	v_lshl_add_u64 v[10:11], s[16:17], 0, v[152:153]
	s_mov_b32 m0, s55
	s_add_u32 s40, s44, 0x41000
	global_load_lds_dwordx4 v[10:11], off
	v_lshl_add_u64 v[10:11], s[16:17], 0, v[154:155]
	s_mov_b32 m0, s56
	s_addc_u32 s41, s45, 0
	global_load_lds_dwordx4 v[10:11], off
	s_add_i32 m0, s51, 0x1c000
	v_lshl_add_u64 v[10:11], s[40:41], 0, v[148:149]
	global_load_lds_dwordx4 v[10:11], off
	v_lshl_add_u64 v[10:11], s[40:41], 0, v[146:147]
	s_add_i32 m0, s51, 0x1e000
	v_lshlrev_b32_e32 v12, 2, v0
	global_load_lds_dwordx4 v[10:11], off
	v_and_b32_e32 v10, 15, v0
	v_lshlrev_b32_e32 v11, 1, v14
	v_lshl_or_b32 v166, s21, 6, v10
	v_lshl_or_b32 v10, v10, 6, v11
	v_and_b32_e32 v12, 32, v12
	v_lshlrev_b32_e32 v13, 6, v0
	s_movk_i32 s21, 0x3c0
	s_waitcnt vmcnt(6)
	v_bitop3_b32 v10, v10, s24, v12 bitop3:0xde
	v_and_or_b32 v11, v13, s21, v11
	s_cmpk_lt_u32 s20, 0x100
	v_bitop3_b32 v167, s36, v11, v12 bitop3:0xf6
	s_mov_b32 s57, 0
	s_cselect_b64 s[20:21], -1, 0
	s_mov_b32 s24, 0x42800000
	s_add_i32 s58, 0, 0x10000
	s_add_i32 s59, 0, 0x14000
	v_add_u32_e32 v168, 0, v10
	s_mov_b32 s36, 0x3c800000
	s_mov_b32 s60, 0xc0c00000
	s_mov_b32 s38, 0xc01d265f
	s_add_i32 s61, s51, 0xc000
	s_add_i32 s62, s51, 0xe000
	v_mov_b32_e32 v169, 0x41000000
	s_mov_b64 s[40:41], s[44:45]
	s_barrier
	s_branch .LBB0_1033

; #define PG8_STAGE(bufoff, gbase, voff) do { _Pragma("unroll") for (int _i = 0; _i < 2; ++_i) \
;         __builtin_amdgcn_global_load_lds((const unsigned*)((const char*)(gbase) + (voff)[_i]), (LAS unsigned*)(lds + (bufoff) + ldsw + _i * 8192), 16, 0, 0); } while (0)
; #define PG8_LDA(dst, b, h) do { _Pragma("unroll") for (int m = 0; m < 4; ++m) { if constexpr (F8) dst##8[m] = PG8_LD32(lds + PG8_SA(b, h) + aoff + m * 2048); \
;         else { _Pragma("unroll") for (int k = 0; k < 2; ++k) dst[m][k] = *(const LAS bf16x8*)(lds + PG8_SA(b, h) + aoff + m * 2048 + k * 1024); } } } while (0)
; #define PG8_LDB(dst, b, h) do { _Pragma("unroll") for (int n = 0; n < 2; ++n) { if constexpr (F8) dst##8[n] = PG8_LD32(lds + PG8_SB(b, h) + boff + n * 2048); \
;         else { _Pragma("unroll") for (int k = 0; k < 2; ++k) dst[n][k] = *(const LAS bf16x8*)(lds + PG8_SB(b, h) + boff + n * 2048 + k * 1024); } } } while (0)
; #define PG8_WAIT_V(n) asm volatile("s_waitcnt vmcnt(" #n ")" ::: "memory")
; template <class Epi, class Sched, bool GATHER, bool F8 = false>
; __device__ __forceinline__ void gemm_phase(LAS unsigned char* lds, const int K, const Sched& S, const Epi& E) {
;     ...
;         const bool has_next = S.next(ui + 1, nxt);
;         const char* nA = has_next ? nxt.A : cA; const char* nB = has_next ? nxt.B : cB;
;         for (int t = 0; t < nt; t += 2) {
;             const bool last = (t == nt - 2);
;             const char* a1 = cA + (size_t)(t + 1) * kstep;
;             const char* a2 = last ? nA : cA + (size_t)(t + 2) * kstep; const char* b2 = last ? nB : cB + (size_t)(t + 2) * kstep;
;             const char* a3 = a2 + kstep; const char* b3 = b2 + kstep;
;             if constexpr (GATHER) { if (last && has_next) S.offsets(ui + 1, RA, CA, vN); }
;             PG8_LDB(B0, 0, 0); PG8_LDB(B1, 0, 1); PG8_SCHED; PG8_LDA(At, 0, 0); PG8_STAGE(PG8_SA(1, 1), a1, vA[1]);
;             PG8_WAIT_V(8); PG8_WAIT_L(0); PG8_BAR; PG8_MMA(0, 0, At, B0); PG8_MMA(0, 1, At, B1); PG8_BAR; PG8_SCHED;
;     __device__ __forceinline__ void init(f32x4 (&acc)[2][2][4][2], const Pre& p) const {
; #pragma unroll
;         for (int ai = 0; ai < 2; ++ai)
; #pragma unroll
;             for (int m = 0; m < 4; ++m)
; #pragma unroll
;                 for (int n = 0; n < 2; ++n) { acc[ai][0][m][n] = p.g[n] * WSCALE; acc[ai][1][m][n] = (p.u[n] + 1.0f) * WSCALE; }
;     }
.LBB0_1035:
	s_lshl_b32 s46, s57, 10
	s_waitcnt vmcnt(0)
	v_pk_add_f32 v[8:9], v[8:9], 1.0 op_sel_hi:[1,0]
	v_pk_add_f32 v[4:5], v[4:5], 1.0 op_sel_hi:[1,0]
	s_add_i32 s46, s46, 0
	v_pk_mul_f32 v[20:21], v[64:65], s[24:25] op_sel_hi:[1,0]
	v_pk_mul_f32 v[12:13], v[60:61], s[24:25] op_sel_hi:[1,0]
	v_pk_add_f32 v[6:7], v[6:7], 1.0 op_sel_hi:[1,0]
	v_pk_mul_f32 v[24:25], v[8:9], s[24:25] op_sel_hi:[1,0]
	v_pk_add_f32 v[2:3], v[2:3], 1.0 op_sel_hi:[1,0]
	v_pk_mul_f32 v[16:17], v[4:5], s[24:25] op_sel_hi:[1,0]
	s_add_i32 s46, s46, 0x20800
	v_pk_mul_f32 v[18:19], v[62:63], s[24:25] op_sel_hi:[1,0]
	v_pk_mul_f32 v[10:11], v[58:59], s[24:25] op_sel_hi:[1,0]
	v_pk_mul_f32 v[22:23], v[6:7], s[24:25] op_sel_hi:[1,0]
	v_pk_mul_f32 v[14:15], v[2:3], s[24:25] op_sel_hi:[1,0]
	s_add_u32 s65, s44, 0x2000
	v_mov_b64_e32 v[28:29], v[16:17]
	v_mov_b64_e32 v[36:37], v[24:25]
	v_mov_b64_e32 v[44:45], v[16:17]
	v_mov_b64_e32 v[52:53], v[24:25]
	v_mov_b64_e32 v[68:69], v[16:17]
	v_mov_b64_e32 v[76:77], v[24:25]
	v_mov_b64_e32 v[32:33], v[12:13]
	v_mov_b64_e32 v[40:41], v[20:21]
	v_mov_b64_e32 v[48:49], v[12:13]
	v_mov_b64_e32 v[56:57], v[20:21]
	v_mov_b64_e32 v[72:73], v[12:13]
	v_mov_b64_e32 v[80:81], v[20:21]
	v_mov_b64_e32 v[84:85], v[16:17]
	v_mov_b64_e32 v[92:93], v[24:25]
	v_mov_b64_e32 v[100:101], v[16:17]
	v_mov_b64_e32 v[108:109], v[24:25]
	v_mov_b64_e32 v[116:117], v[16:17]
	v_mov_b64_e32 v[124:125], v[24:25]
	v_mov_b64_e32 v[132:133], v[16:17]
	v_mov_b64_e32 v[140:141], v[24:25]
	v_mov_b64_e32 v[88:89], v[12:13]
	v_mov_b64_e32 v[96:97], v[20:21]
	v_mov_b64_e32 v[104:105], v[12:13]
	v_mov_b64_e32 v[112:113], v[20:21]
	v_mov_b64_e32 v[120:121], v[12:13]
	v_mov_b64_e32 v[128:129], v[20:21]
	v_mov_b64_e32 v[136:137], v[12:13]
	v_mov_b64_e32 v[144:145], v[20:21]
	v_mov_b32_e32 v58, v163
	v_mov_b32_e32 v59, v153
	v_mov_b32_e32 v60, v164
	v_mov_b32_e32 v61, v153
	v_lshl_add_u32 v151, v160, 2, s46
	v_lshl_add_u32 v171, v161, 2, s46
	s_addc_u32 s66, s45, 0
	s_mov_b32 s67, -2
	s_mov_b64 s[44:45], s[16:17]
	v_mov_b64_e32 v[26:27], v[14:15]
	v_mov_b64_e32 v[34:35], v[22:23]
	v_mov_b64_e32 v[42:43], v[14:15]
	v_mov_b64_e32 v[50:51], v[22:23]
	v_mov_b64_e32 v[66:67], v[14:15]
	v_mov_b64_e32 v[74:75], v[22:23]
	v_mov_b64_e32 v[30:31], v[10:11]
	v_mov_b64_e32 v[38:39], v[18:19]
	v_mov_b64_e32 v[46:47], v[10:11]
	v_mov_b64_e32 v[54:55], v[18:19]
	v_mov_b64_e32 v[70:71], v[10:11]
	v_mov_b64_e32 v[78:79], v[18:19]
	v_mov_b64_e32 v[82:83], v[14:15]
	v_mov_b64_e32 v[90:91], v[22:23]
	v_mov_b64_e32 v[98:99], v[14:15]
	v_mov_b64_e32 v[106:107], v[22:23]
	v_mov_b64_e32 v[114:115], v[14:15]
	v_mov_b64_e32 v[122:123], v[22:23]
	v_mov_b64_e32 v[130:131], v[14:15]
	v_mov_b64_e32 v[138:139], v[22:23]
	v_mov_b64_e32 v[86:87], v[10:11]
	v_mov_b64_e32 v[94:95], v[18:19]
	v_mov_b64_e32 v[102:103], v[10:11]
	v_mov_b64_e32 v[110:111], v[18:19]
	v_mov_b64_e32 v[118:119], v[10:11]
	v_mov_b64_e32 v[126:127], v[18:19]
	v_mov_b64_e32 v[134:135], v[10:11]
	v_mov_b64_e32 v[142:143], v[18:19]
	s_branch .LBB0_1037
.LBB0_1036:
	v_add_u32_e32 v62, s58, v167
	ds_read_b128 v[2:5], v62
	ds_read_b128 v[6:9], v62 offset:1024
	ds_read_b128 v[172:175], v62 offset:2048
	ds_read_b128 v[176:179], v62 offset:3072
	v_add_u32_e32 v62, s59, v167
	ds_read_b128 v[180:183], v62
	ds_read_b128 v[184:187], v62 offset:1024
	ds_read_b128 v[188:191], v62 offset:2048
	ds_read_b128 v[192:195], v62 offset:3072
	s_add_u32 s48, s44, 0x80
	s_addc_u32 s49, s45, 0
	s_and_b64 s[46:47], s[46:47], exec
	s_cselect_b32 s49, s1, s49
	s_cselect_b32 s48, s0, s48
	s_cselect_b32 s47, s41, s66
	s_cselect_b32 s46, s40, s65
	s_mov_b32 m0, s61
	v_lshl_add_u64 v[62:63], s[44:45], 0, v[58:59]
	ds_read_b128 v[196:199], v168
	ds_read_b128 v[200:203], v168 offset:1024
	ds_read_b128 v[204:207], v168 offset:2048
	ds_read_b128 v[208:211], v168 offset:3072
	ds_read_b128 v[212:215], v168 offset:4096
	ds_read_b128 v[216:219], v168 offset:5120
	ds_read_b128 v[220:223], v168 offset:6144
	ds_read_b128 v[224:227], v168 offset:7168
	global_load_lds_dwordx4 v[62:63], off
	v_lshl_add_u64 v[62:63], s[44:45], 0, v[60:61]
	s_mov_b32 m0, s62
	s_nop 0
	global_load_lds_dwordx4 v[62:63], off
	s_waitcnt vmcnt(8)
	s_waitcnt lgkmcnt(0)
	s_barrier
	s_setprio 1
	s_waitcnt lgkmcnt(0)
	v_mfma_scale_f32_16x16x128_f8f6f4 v[142:145], v[2:9], v[196:203], v[142:145], v165, v165 op_sel_hi:[0,0,0]
	v_mfma_scale_f32_16x16x128_f8f6f4 v[134:137], v[172:179], v[196:203], v[134:137], v165, v165 op_sel_hi:[0,0,0]
	v_mfma_scale_f32_16x16x128_f8f6f4 v[126:129], v[2:9], v[204:211], v[126:129], v165, v165 op_sel_hi:[0,0,0]
	v_mfma_scale_f32_16x16x128_f8f6f4 v[118:121], v[172:179], v[204:211], v[118:121], v165, v165 op_sel_hi:[0,0,0]
	v_mfma_scale_f32_16x16x128_f8f6f4 v[110:113], v[2:9], v[212:219], v[110:113], v165, v165 op_sel_hi:[0,0,0]
	v_mfma_scale_f32_16x16x128_f8f6f4 v[102:105], v[172:179], v[212:219], v[102:105], v165, v165 op_sel_hi:[0,0,0]
	v_mfma_scale_f32_16x16x128_f8f6f4 v[94:97], v[2:9], v[220:227], v[94:97], v165, v165 op_sel_hi:[0,0,0]
	v_mfma_scale_f32_16x16x128_f8f6f4 v[86:89], v[172:179], v[220:227], v[86:89], v165, v165 op_sel_hi:[0,0,0]
	s_setprio 0
	s_setprio 1
	v_mfma_scale_f32_16x16x128_f8f6f4 v[138:141], v[180:187], v[196:203], v[138:141], v165, v165 op_sel_hi:[0,0,0]
	v_mfma_scale_f32_16x16x128_f8f6f4 v[130:133], v[188:195], v[196:203], v[130:133], v165, v165 op_sel_hi:[0,0,0]
	v_mfma_scale_f32_16x16x128_f8f6f4 v[122:125], v[180:187], v[204:211], v[122:125], v165, v165 op_sel_hi:[0,0,0]
	v_mfma_scale_f32_16x16x128_f8f6f4 v[114:117], v[188:195], v[204:211], v[114:117], v165, v165 op_sel_hi:[0,0,0]
	v_mfma_scale_f32_16x16x128_f8f6f4 v[106:109], v[180:187], v[212:219], v[106:109], v165, v165 op_sel_hi:[0,0,0]
	v_mfma_scale_f32_16x16x128_f8f6f4 v[98:101], v[188:195], v[212:219], v[98:101], v165, v165 op_sel_hi:[0,0,0]
	v_mfma_scale_f32_16x16x128_f8f6f4 v[90:93], v[180:187], v[220:227], v[90:93], v165, v165 op_sel_hi:[0,0,0]
	v_mfma_scale_f32_16x16x128_f8f6f4 v[82:85], v[188:195], v[220:227], v[82:85], v165, v165 op_sel_hi:[0,0,0]
	s_setprio 0
	s_barrier
; #define PG8_STAGE(bufoff, gbase, voff) do { _Pragma("unroll") for (int _i = 0; _i < 2; ++_i) \
;         __builtin_amdgcn_global_load_lds((const unsigned*)((const char*)(gbase) + (voff)[_i]), (LAS unsigned*)(lds + (bufoff) + ldsw + _i * 8192), 16, 0, 0); } while (0)
; #define PG8_LDA(dst, b, h) do { _Pragma("unroll") for (int m = 0; m < 4; ++m) { if constexpr (F8) dst##8[m] = PG8_LD32(lds + PG8_SA(b, h) + aoff + m * 2048); \
;         else { _Pragma("unroll") for (int k = 0; k < 2; ++k) dst[m][k] = *(const LAS bf16x8*)(lds + PG8_SA(b, h) + aoff + m * 2048 + k * 1024); } } } while (0)
; #define PG8_LDB(dst, b, h) do { _Pragma("unroll") for (int n = 0; n < 2; ++n) { if constexpr (F8) dst##8[n] = PG8_LD32(lds + PG8_SB(b, h) + boff + n * 2048); \
;         else { _Pragma("unroll") for (int k = 0; k < 2; ++k) dst[n][k] = *(const LAS bf16x8*)(lds + PG8_SB(b, h) + boff + n * 2048 + k * 1024); } } } while (0)
; #define PG8_WAIT_V(n) asm volatile("s_waitcnt vmcnt(" #n ")" ::: "memory")
; #define PG8_WAIT_L(n) asm volatile("s_waitcnt lgkmcnt(" #n ")" ::: "memory")
; #define PG8_BAR __builtin_amdgcn_s_barrier()
; #define PG8_SCHED __builtin_amdgcn_sched_barrier(0)
; template <class Epi, class Sched, bool GATHER, bool F8 = false>
; __device__ __forceinline__ void gemm_phase(LAS unsigned char* lds, const int K, const Sched& S, const Epi& E) {
;     ...
;             PG8_LDA(At, 0, 1); PG8_STAGE(PG8_SB(0, 0), b2, voffB); PG8_STAGE(PG8_SB(0, 1), b2 + hstepB, voffB); PG8_STAGE(PG8_SA(0, 0), a2, vN[0]);
;             PG8_WAIT_V(8); PG8_WAIT_L(0); PG8_BAR; PG8_MMA(1, 0, At, B0); PG8_MMA(1, 1, At, B1); PG8_BAR; PG8_SCHED;
;             PG8_LDB(B0, 1, 0); PG8_LDB(B1, 1, 1); PG8_SCHED; PG8_LDA(At, 1, 0); PG8_STAGE(PG8_SA(0, 1), a2, vN[1]);
;             PG8_WAIT_V(8); PG8_WAIT_L(0); PG8_BAR; PG8_MMA(0, 0, At, B0); PG8_MMA(0, 1, At, B1); PG8_BAR; PG8_SCHED;
	s_add_i32 s68, s58, s37
	v_lshl_add_u64 v[62:63], s[46:47], 0, v[148:149]
	s_mov_b32 m0, s68
	ds_read_b128 v[196:199], v168 offset:16384
	ds_read_b128 v[200:203], v168 offset:17408
	ds_read_b128 v[204:207], v168 offset:18432
	ds_read_b128 v[208:211], v168 offset:19456
	ds_read_b128 v[212:215], v168 offset:20480
	ds_read_b128 v[216:219], v168 offset:21504
	ds_read_b128 v[220:223], v168 offset:22528
	ds_read_b128 v[224:227], v168 offset:23552
	global_load_lds_dwordx4 v[62:63], off
	s_add_i32 m0, s68, 0x2000
	s_add_u32 s68, s46, 0x40000
	v_lshl_add_u64 v[64:65], s[46:47], 0, v[146:147]
	s_addc_u32 s69, s47, 0
	s_add_i32 s70, s59, s37
	global_load_lds_dwordx4 v[64:65], off
	v_lshl_add_u64 v[156:157], s[68:69], 0, v[148:149]
	s_mov_b32 m0, s70
	v_mov_b32_e32 v155, v153
	global_load_lds_dwordx4 v[156:157], off
	v_lshl_add_u64 v[156:157], s[68:69], 0, v[146:147]
	s_add_i32 m0, s70, 0x2000
	v_lshl_add_u64 v[158:159], s[48:49], 0, v[152:153]
	global_load_lds_dwordx4 v[156:157], off
	s_mov_b32 m0, s51
	v_lshl_add_u64 v[156:157], s[48:49], 0, v[154:155]
	global_load_lds_dwordx4 v152, s[48:49]
	s_mov_b32 m0, s52
	s_nop 0
	global_load_lds_dwordx4 v154, s[48:49]
	s_waitcnt vmcnt(8)
	s_waitcnt lgkmcnt(0)
	s_barrier
	s_setprio 1
	s_waitcnt lgkmcnt(0)
	v_mfma_scale_f32_16x16x128_f8f6f4 v[78:81], v[2:9], v[196:203], v[78:81], v165, v165 op_sel_hi:[0,0,0]
	v_mfma_scale_f32_16x16x128_f8f6f4 v[70:73], v[172:179], v[196:203], v[70:73], v165, v165 op_sel_hi:[0,0,0]
	v_mfma_scale_f32_16x16x128_f8f6f4 v[54:57], v[2:9], v[204:211], v[54:57], v165, v165 op_sel_hi:[0,0,0]
	v_mfma_scale_f32_16x16x128_f8f6f4 v[46:49], v[172:179], v[204:211], v[46:49], v165, v165 op_sel_hi:[0,0,0]
	v_mfma_scale_f32_16x16x128_f8f6f4 v[38:41], v[2:9], v[212:219], v[38:41], v165, v165 op_sel_hi:[0,0,0]
	v_mfma_scale_f32_16x16x128_f8f6f4 v[30:33], v[172:179], v[212:219], v[30:33], v165, v165 op_sel_hi:[0,0,0]
	v_mfma_scale_f32_16x16x128_f8f6f4 v[18:21], v[2:9], v[220:227], v[18:21], v165, v165 op_sel_hi:[0,0,0]
	v_mfma_scale_f32_16x16x128_f8f6f4 v[10:13], v[172:179], v[220:227], v[10:13], v165, v165 op_sel_hi:[0,0,0]
	s_setprio 0
	s_setprio 1
	v_mfma_scale_f32_16x16x128_f8f6f4 v[74:77], v[180:187], v[196:203], v[74:77], v165, v165 op_sel_hi:[0,0,0]
	v_mfma_scale_f32_16x16x128_f8f6f4 v[66:69], v[188:195], v[196:203], v[66:69], v165, v165 op_sel_hi:[0,0,0]
	v_mfma_scale_f32_16x16x128_f8f6f4 v[50:53], v[180:187], v[204:211], v[50:53], v165, v165 op_sel_hi:[0,0,0]
	v_mfma_scale_f32_16x16x128_f8f6f4 v[42:45], v[188:195], v[204:211], v[42:45], v165, v165 op_sel_hi:[0,0,0]
	v_mfma_scale_f32_16x16x128_f8f6f4 v[34:37], v[180:187], v[212:219], v[34:37], v165, v165 op_sel_hi:[0,0,0]
	v_mfma_scale_f32_16x16x128_f8f6f4 v[26:29], v[188:195], v[212:219], v[26:29], v165, v165 op_sel_hi:[0,0,0]
	v_mfma_scale_f32_16x16x128_f8f6f4 v[22:25], v[180:187], v[220:227], v[22:25], v165, v165 op_sel_hi:[0,0,0]
	v_mfma_scale_f32_16x16x128_f8f6f4 v[14:17], v[188:195], v[220:227], v[14:17], v165, v165 op_sel_hi:[0,0,0]
	s_setprio 0
	s_barrier
	s_add_i32 s68, 0, 0x18000
	s_add_i32 s69, 0, 0x1c000
	v_add_u32_e32 v2, s68, v167
	v_add_u32_e32 v155, s69, v167
	ds_read_b128 v[172:175], v2
	ds_read_b128 v[176:179], v2 offset:1024
	ds_read_b128 v[180:183], v2 offset:2048
	ds_read_b128 v[184:187], v2 offset:3072
	ds_read_b128 v[2:5], v155
	ds_read_b128 v[6:9], v155 offset:1024
	ds_read_b128 v[188:191], v155 offset:2048
	ds_read_b128 v[192:195], v155 offset:3072
	s_mov_b32 m0, s53
	ds_read_b128 v[196:199], v168 offset:32768
	ds_read_b128 v[200:203], v168 offset:33792
	ds_read_b128 v[204:207], v168 offset:34816
	ds_read_b128 v[208:211], v168 offset:35840
	ds_read_b128 v[212:215], v168 offset:36864
	ds_read_b128 v[216:219], v168 offset:37888
	ds_read_b128 v[220:223], v168 offset:38912
	ds_read_b128 v[224:227], v168 offset:39936
	global_load_lds_dwordx4 v163, s[48:49]
	s_mov_b32 m0, s54
	s_nop 0
	global_load_lds_dwordx4 v164, s[48:49]
	s_waitcnt vmcnt(8)
	s_waitcnt lgkmcnt(0)
	s_barrier
; #define PG8_STAGE(bufoff, gbase, voff) do { _Pragma("unroll") for (int _i = 0; _i < 2; ++_i) \
;         __builtin_amdgcn_global_load_lds((const unsigned*)((const char*)(gbase) + (voff)[_i]), (LAS unsigned*)(lds + (bufoff) + ldsw + _i * 8192), 16, 0, 0); } while (0)
; #define PG8_LDA(dst, b, h) do { _Pragma("unroll") for (int m = 0; m < 4; ++m) { if constexpr (F8) dst##8[m] = PG8_LD32(lds + PG8_SA(b, h) + aoff + m * 2048); \
;         else { _Pragma("unroll") for (int k = 0; k < 2; ++k) dst[m][k] = *(const LAS bf16x8*)(lds + PG8_SA(b, h) + aoff + m * 2048 + k * 1024); } } } while (0)
; #define PG8_WAIT_V(n) asm volatile("s_waitcnt vmcnt(" #n ")" ::: "memory")
; #define PG8_WAIT_L(n) asm volatile("s_waitcnt lgkmcnt(" #n ")" ::: "memory")
; #define PG8_BAR __builtin_amdgcn_s_barrier()
; #define PG8_SCHED __builtin_amdgcn_sched_barrier(0)
; template <class Epi, class Sched, bool GATHER, bool F8 = false>
; __device__ __forceinline__ void gemm_phase(LAS unsigned char* lds, const int K, const Sched& S, const Epi& E) {
;     ...
;             PG8_WAIT_V(8); PG8_WAIT_L(0); PG8_BAR; PG8_MMA(0, 0, At, B0); PG8_MMA(0, 1, At, B1); PG8_BAR; PG8_SCHED;
;             PG8_LDA(At, 1, 1); PG8_STAGE(PG8_SB(1, 0), b3, voffB); PG8_STAGE(PG8_SB(1, 1), b3 + hstepB, voffB); PG8_STAGE(PG8_SA(1, 0), a3, vN[0]);
;             PG8_WAIT_V(8); PG8_WAIT_L(0); PG8_BAR; PG8_MMA(1, 0, At, B0); PG8_MMA(1, 1, At, B1); PG8_BAR; PG8_SCHED;
;         }
	s_setprio 1
	s_waitcnt lgkmcnt(0)
	v_mfma_scale_f32_16x16x128_f8f6f4 v[142:145], v[172:179], v[196:203], v[142:145], v165, v165 op_sel_hi:[0,0,0]
	v_mfma_scale_f32_16x16x128_f8f6f4 v[134:137], v[180:187], v[196:203], v[134:137], v165, v165 op_sel_hi:[0,0,0]
	v_mfma_scale_f32_16x16x128_f8f6f4 v[126:129], v[172:179], v[204:211], v[126:129], v165, v165 op_sel_hi:[0,0,0]
	v_mfma_scale_f32_16x16x128_f8f6f4 v[118:121], v[180:187], v[204:211], v[118:121], v165, v165 op_sel_hi:[0,0,0]
	v_mfma_scale_f32_16x16x128_f8f6f4 v[110:113], v[172:179], v[212:219], v[110:113], v165, v165 op_sel_hi:[0,0,0]
	v_mfma_scale_f32_16x16x128_f8f6f4 v[102:105], v[180:187], v[212:219], v[102:105], v165, v165 op_sel_hi:[0,0,0]
	v_mfma_scale_f32_16x16x128_f8f6f4 v[94:97], v[172:179], v[220:227], v[94:97], v165, v165 op_sel_hi:[0,0,0]
	v_mfma_scale_f32_16x16x128_f8f6f4 v[86:89], v[180:187], v[220:227], v[86:89], v165, v165 op_sel_hi:[0,0,0]
	s_setprio 0
	s_setprio 1
	v_mfma_scale_f32_16x16x128_f8f6f4 v[138:141], v[2:9], v[196:203], v[138:141], v165, v165 op_sel_hi:[0,0,0]
	v_mfma_scale_f32_16x16x128_f8f6f4 v[130:133], v[188:195], v[196:203], v[130:133], v165, v165 op_sel_hi:[0,0,0]
	v_mfma_scale_f32_16x16x128_f8f6f4 v[122:125], v[2:9], v[204:211], v[122:125], v165, v165 op_sel_hi:[0,0,0]
	v_mfma_scale_f32_16x16x128_f8f6f4 v[114:117], v[188:195], v[204:211], v[114:117], v165, v165 op_sel_hi:[0,0,0]
	v_mfma_scale_f32_16x16x128_f8f6f4 v[106:109], v[2:9], v[212:219], v[106:109], v165, v165 op_sel_hi:[0,0,0]
	v_mfma_scale_f32_16x16x128_f8f6f4 v[98:101], v[188:195], v[212:219], v[98:101], v165, v165 op_sel_hi:[0,0,0]
	v_mfma_scale_f32_16x16x128_f8f6f4 v[90:93], v[2:9], v[220:227], v[90:93], v165, v165 op_sel_hi:[0,0,0]
	v_mfma_scale_f32_16x16x128_f8f6f4 v[82:85], v[188:195], v[220:227], v[82:85], v165, v165 op_sel_hi:[0,0,0]
	s_setprio 0
	s_barrier
	s_add_i32 s48, s68, s37
	v_lshl_add_u64 v[62:63], v[62:63], 0, s[100:101]
	s_mov_b32 m0, s48
	ds_read_b128 v[196:199], v168 offset:49152
	ds_read_b128 v[200:203], v168 offset:50176
	ds_read_b128 v[204:207], v168 offset:51200
	ds_read_b128 v[208:211], v168 offset:52224
	ds_read_b128 v[212:215], v168 offset:53248
	ds_read_b128 v[216:219], v168 offset:54272
	ds_read_b128 v[220:223], v168 offset:55296
	ds_read_b128 v[224:227], v168 offset:56320
	global_load_lds_dwordx4 v[62:63], off
	s_add_i32 m0, s48, 0x2000
	s_add_u32 s46, s46, 0x41000
	v_lshl_add_u64 v[62:63], v[64:65], 0, s[100:101]
	s_addc_u32 s47, s47, 0
	s_add_i32 s48, s69, s37
	global_load_lds_dwordx4 v[62:63], off
	v_lshl_add_u64 v[62:63], s[46:47], 0, v[148:149]
	s_mov_b32 m0, s48
	s_nop 0
	global_load_lds_dwordx4 v[62:63], off
	v_lshl_add_u64 v[62:63], s[46:47], 0, v[146:147]
	s_add_i32 m0, s48, 0x2000
	s_nop 0
	global_load_lds_dwordx4 v[62:63], off
	v_lshl_add_u64 v[62:63], v[158:159], 0, s[14:15]
	s_mov_b32 m0, s55
	s_nop 0
	global_load_lds_dwordx4 v[62:63], off
	v_lshl_add_u64 v[62:63], v[156:157], 0, s[14:15]
	s_mov_b32 m0, s56
	s_nop 0
	global_load_lds_dwordx4 v[62:63], off
	s_waitcnt vmcnt(8)
	s_waitcnt lgkmcnt(0)
	s_barrier
	s_setprio 1
	s_waitcnt lgkmcnt(0)
	v_mfma_scale_f32_16x16x128_f8f6f4 v[78:81], v[172:179], v[196:203], v[78:81], v165, v165 op_sel_hi:[0,0,0]
	v_mfma_scale_f32_16x16x128_f8f6f4 v[70:73], v[180:187], v[196:203], v[70:73], v165, v165 op_sel_hi:[0,0,0]
	v_mfma_scale_f32_16x16x128_f8f6f4 v[54:57], v[172:179], v[204:211], v[54:57], v165, v165 op_sel_hi:[0,0,0]
	v_mfma_scale_f32_16x16x128_f8f6f4 v[46:49], v[180:187], v[204:211], v[46:49], v165, v165 op_sel_hi:[0,0,0]
	v_mfma_scale_f32_16x16x128_f8f6f4 v[38:41], v[172:179], v[212:219], v[38:41], v165, v165 op_sel_hi:[0,0,0]
	v_mfma_scale_f32_16x16x128_f8f6f4 v[30:33], v[180:187], v[212:219], v[30:33], v165, v165 op_sel_hi:[0,0,0]
	v_mfma_scale_f32_16x16x128_f8f6f4 v[18:21], v[172:179], v[220:227], v[18:21], v165, v165 op_sel_hi:[0,0,0]
	v_mfma_scale_f32_16x16x128_f8f6f4 v[10:13], v[180:187], v[220:227], v[10:13], v165, v165 op_sel_hi:[0,0,0]
	s_setprio 0
	s_setprio 1
	v_mfma_scale_f32_16x16x128_f8f6f4 v[74:77], v[2:9], v[196:203], v[74:77], v165, v165 op_sel_hi:[0,0,0]
	v_mfma_scale_f32_16x16x128_f8f6f4 v[66:69], v[188:195], v[196:203], v[66:69], v165, v165 op_sel_hi:[0,0,0]
	v_mfma_scale_f32_16x16x128_f8f6f4 v[50:53], v[2:9], v[204:211], v[50:53], v165, v165 op_sel_hi:[0,0,0]
	v_mfma_scale_f32_16x16x128_f8f6f4 v[42:45], v[188:195], v[204:211], v[42:45], v165, v165 op_sel_hi:[0,0,0]
	v_mfma_scale_f32_16x16x128_f8f6f4 v[34:37], v[2:9], v[212:219], v[34:37], v165, v165 op_sel_hi:[0,0,0]
	v_mfma_scale_f32_16x16x128_f8f6f4 v[26:29], v[188:195], v[212:219], v[26:29], v165, v165 op_sel_hi:[0,0,0]
	v_mfma_scale_f32_16x16x128_f8f6f4 v[22:25], v[2:9], v[220:227], v[22:25], v165, v165 op_sel_hi:[0,0,0]
	v_mfma_scale_f32_16x16x128_f8f6f4 v[14:17], v[188:195], v[220:227], v[14:17], v165, v165 op_sel_hi:[0,0,0]
	s_setprio 0
	s_barrier
	s_add_i32 s67, s67, 2
	s_add_u32 s44, s44, 0x100
	s_addc_u32 s45, s45, 0
	s_add_u32 s65, s65, 0x2000
	s_addc_u32 s66, s66, 0
	s_cmp_gt_u32 s67, 13
	s_cbranch_scc1 .LBB0_1039

; #define PG8_BAR __builtin_amdgcn_s_barrier()
; template <class Epi, class Sched, bool GATHER, bool F8 = false>
; __device__ __forceinline__ void gemm_phase(LAS unsigned char* lds, const int K, const Sched& S, const Epi& E) {
;     ...
;     for (int i = 0; i < 2; ++i) { int R, C; stage_rc(tid * 16 + i * 8192, R, C); const int Rb = epi_wide<Epi>() ? (64 * (R >> 5) + perm32(R & 31)) : (Epi::PERM ? ((R & ~31) + perm32(R & 31)) : R);
;         RA[i] = R; CA[i] = C; voffB[i] = (unsigned)(Rb * K + C) * 2u;
;         vA[0][i] = (unsigned)(R * K + C) * 2u; vA[1][i] = vA[0][i] + (unsigned)hstep; }
;     const unsigned ldsw = (unsigned)wid * 1024u;
;     const int aoff = lds_byte(wr * 64 + fr, fq * 8), boff = lds_byte(wc * 32 + fr, fq * 8);
;     ...
;     Unit cur, nxt; int ui = 0;
;     if (!S.next(0, cur)) return;
;     if constexpr (GATHER) { S.offsets(0, RA, CA, vA); }
; #pragma unroll
;     for (int h = 0; h < 2; ++h)
; #pragma unroll
;         for (int i = 0; i < 2; ++i) vN[h][i] = vA[h][i];
;     f32x4 acc[2][2][4][2];
; #pragma unroll
;     for (int a = 0; a < 2; ++a)
; #pragma unroll
;         for (int b = 0; b < 2; ++b)
; #pragma unroll
;             for (int m = 0; m < 4; ++m)
; #pragma unroll
;                 for (int n = 0; n < 2; ++n) acc[a][b][m][n] = (f32x4){0.f, 0.f, 0.f, 0.f};
;     if constexpr (EpiInit<Epi>::value) { const typename EpiInit<Epi>::Pre p0 = E.preload(cur, wr, wc, fr, fq); E.init(acc, p0); }
;     int one_scale = 0x7f7f7f7f; asm volatile("" : "+v"(one_scale));
;     bf16x8 At[4][2], B0[2][2], B1[2][2]; i32x8 At8[4], B08[2], B18[2];
;     const char* cA = cur.A; const char* cB = cur.B;
;     PG8_STAGE(PG8_SB(0, 0), cB, voffB); PG8_STAGE(PG8_SB(0, 1), cB + hstepB, voffB); PG8_STAGE(PG8_SA(0, 0), cA, vA[0]); PG8_STAGE(PG8_SA(0, 1), cA, vA[1]);
;     if (wr == 1) PG8_BAR;
;     PG8_WAIT_V(2); PG8_BAR;
;     PG8_STAGE(PG8_SB(1, 0), cB + kstep, voffB); PG8_STAGE(PG8_SA(1, 0), cA + kstep, vA[0]); PG8_STAGE(PG8_SB(1, 1), cB + hstepB + kstep, voffB);
;     __device__ __forceinline__ Pre preload(const Unit& u, int wr, int wc, int fr, int fq) const {
;         const float* pb = bd + (size_t)u.tag * DM + u.col0 + wc * 64 + 8 * fq;
;         Pre p;
; #pragma unroll
;         for (int bj = 0; bj < 2; ++bj)
; #pragma unroll
;             for (int n = 0; n < 2; ++n) p.bv[bj][n] = *(const f32x4*)(pb + bj * 32 + 4 * n);
;         return p;
;     }
.LBB0_1119:
	s_add_i32 s0, 0, 0x20600
	v_mov_b32_e32 v1, s0
	ds_read_b32 v1, v1
	s_lshl_b32 s0, s2, 2
	s_and_b32 s0, s0, 28
	s_bfe_u32 s1, s2, 0x20003
	s_or_b32 s6, s0, s1
	s_waitcnt lgkmcnt(0)
	v_cmp_ge_i32_e32 vcc, s6, v1
	v_readfirstlane_b32 s20, v0
	s_cbranch_vccnz .LBB0_1135
	s_add_u32 s7, s82, 0x34000000
	s_addc_u32 s23, s83, 0
	s_add_u32 s18, s82, 0x24000000
	s_waitcnt vmcnt(0)
	v_lshlrev_b32_e32 v2, 4, v0
	s_addc_u32 s22, s83, 0
	s_lshr_b32 s0, s20, 6
	v_or_b32_e32 v18, 0x2000, v2
	v_and_b32_e32 v5, 32, v0
	s_lshl_b32 s25, s0, 10
	v_lshrrev_b32_e32 v3, 7, v18
	v_bfe_u32 v21, v0, 2, 4
	s_movk_i32 s0, 0x70
	v_bitop3_b32 v19, v2, v5, 48 bitop3:0x6c
	v_and_b32_e32 v20, 64, v0
	v_and_or_b32 v3, v3, s0, v21
	v_or_b32_e32 v2, v19, v20
	v_lshl_or_b32 v146, v3, 11, v2
	v_lshrrev_b32_e32 v3, 5, v0
	v_lshrrev_b32_e32 v6, 1, v0
	v_and_b32_e32 v3, 4, v3
	v_bfe_u32 v5, v0, 2, 2
	v_and_b32_e32 v6, 24, v6
	v_or3_b32 v3, v3, v5, v6
	v_lshrrev_b32_e32 v5, 6, v18
	s_movk_i32 s0, 0xc0
	v_and_or_b32 v5, v5, s0, v3
	s_lshl_b32 s0, s6, 2
	s_add_i32 s0, s0, 0
	s_add_i32 s0, s0, 0x20000
	v_mov_b32_e32 v6, s0
	ds_read_b32 v6, v6
	s_bfe_u32 s16, s20, 0x20006
	s_lshr_b32 s17, s20, 8
	s_lshl_b32 s0, s6, 19
	v_lshrrev_b32_e32 v4, 2, v0
	s_waitcnt lgkmcnt(0)
	v_readfirstlane_b32 s12, v6
	s_ashr_i32 s13, s12, 31
	s_add_u32 s44, s7, s0
	s_addc_u32 s45, s23, 0
	s_lshl_b32 s0, s2, 3
	s_and_b32 s0, s0, 0xffffff00
	s_ashr_i32 s1, s0, 31
	s_lshl_b64 s[2:3], s[12:13], 22
	s_lshl_b64 s[4:5], s[0:1], 11
	s_add_u32 s2, s18, s2
	s_addc_u32 s3, s22, s3
	s_add_u32 s46, s2, s4
	s_addc_u32 s47, s3, s5
	s_lshl_b64 s[2:3], s[12:13], 13
	s_add_u32 s13, s26, s2
	s_addc_u32 s14, s27, s3
	s_lshl_b64 s[2:3], s[0:1], 2
	s_add_u32 s1, s13, s2
	s_addc_u32 s3, s14, s3
	s_lshl_b32 s50, s16, 6
	s_lshl_b32 s2, s16, 8
	s_add_u32 s2, s1, s2
	v_bfe_u32 v22, v0, 4, 2
	v_lshl_or_b32 v150, v5, 11, v2
	v_bfe_u32 v254, v150, 11, 5
	v_and_b32_e32 v150, 0xffff007f, v150
	v_lshl_or_b32 v150, v254, 7, v150
	v_lshrrev_b32_e32 v5, 3, v0
	v_and_or_b32 v3, v4, 64, v3
	s_addc_u32 s3, s3, 0
	s_add_i32 s51, s25, 0
	v_and_or_b32 v5, v5, 48, v21
	v_lshl_or_b32 v156, v3, 11, v2
	v_bfe_u32 v254, v156, 11, 5
	v_and_b32_e32 v156, 0xffff007f, v156
	v_lshl_or_b32 v156, v254, 7, v156
	v_lshlrev_b32_e32 v10, 5, v22
	v_mov_b32_e32 v162, 0x7f7f7f7f
	s_add_i32 m0, s51, 0x10000
	v_lshl_or_b32 v152, v5, 11, v2
	global_load_dwordx4 v[74:77], v10, s[2:3] offset:16
	global_load_dwordx4 v[78:81], v10, s[2:3]
	global_load_dwordx4 v[2:5], v10, s[2:3] offset:144
	global_load_dwordx4 v[6:9], v10, s[2:3] offset:128
	global_load_lds_dwordx4 v156, s[46:47]
	s_add_i32 m0, s51, 0x12000
	s_add_u32 s2, s46, 0x10000
	global_load_lds_dwordx4 v150, s[46:47]
	s_addc_u32 s3, s47, 0
	s_add_i32 m0, s51, 0x14000
	s_add_i32 s52, s51, 0x2000
	global_load_lds_dwordx4 v156, s[2:3]
	s_add_i32 m0, s51, 0x16000
	s_add_i32 s53, s51, 0x4000
	global_load_lds_dwordx4 v150, s[2:3]
	s_mov_b32 m0, s51
	v_or_b32_e32 v154, 0x40000, v152
	global_load_lds_dwordx4 v152, s[44:45]
	s_mov_b32 m0, s52
	s_add_i32 s54, s51, 0x6000
	global_load_lds_dwordx4 v146, s[44:45]
	s_mov_b32 m0, s53
	v_or_b32_e32 v148, 0x40000, v146
	global_load_lds_dwordx4 v154, s[44:45]
	s_mov_b32 m0, s54
	v_mov_b32_e32 v157, 0
	global_load_lds_dwordx4 v148, s[44:45]
	v_mov_b32_e32 v151, v157
	v_mov_b32_e32 v153, v157
	v_mov_b32_e32 v147, v157
	s_cmp_eq_u32 s17, 1
	v_lshlrev_b32_e32 v23, 3, v22
	v_lshl_add_u64 v[16:17], s[46:47], 0, v[156:157]
	v_lshl_add_u64 v[14:15], s[46:47], 0, v[150:151]
	v_lshl_add_u64 v[10:11], s[44:45], 0, v[152:153]
	s_cselect_b64 s[2:3], -1, 0
	s_cmp_lg_u32 s17, 1
	v_lshl_add_u64 v[12:13], s[44:45], 0, v[146:147]
	s_cbranch_scc1 .LBB0_1122
	s_barrier
.LBB0_1122:
	s_lshl_b32 s64, s6, 8
	s_add_u32 s14, s82, 0x44600000
	s_addc_u32 s15, s83, 0
	s_lshl_b32 s55, s17, 6
	s_lshl_b32 s1, s17, 13
	s_lshl_b32 s13, s16, 12
	s_mov_b64 s[16:17], 0x80
	s_mov_b64 s[100:101], 0x1000
	s_add_i32 m0, s51, 0x18000
	v_lshl_add_u64 v[16:17], v[16:17], 0, s[100:101]
	s_waitcnt vmcnt(2)
	s_barrier
	global_load_lds_dwordx4 v[16:17], off
	v_lshl_add_u64 v[14:15], v[14:15], 0, s[100:101]
	s_add_i32 m0, s51, 0x1a000
	s_add_i32 s56, s51, 0x8000
	s_add_i32 s57, s51, 0xa000
	global_load_lds_dwordx4 v[14:15], off
	v_lshl_add_u64 v[10:11], v[10:11], 0, s[16:17]
	s_mov_b32 m0, s56
	s_add_u32 s36, s46, 0x11000
	global_load_lds_dwordx4 v[10:11], off
	v_lshl_add_u64 v[10:11], v[12:13], 0, s[16:17]
	s_mov_b32 m0, s57
	s_addc_u32 s37, s47, 0
	global_load_lds_dwordx4 v[10:11], off
	s_add_i32 m0, s51, 0x1c000
	v_lshl_add_u64 v[10:11], s[36:37], 0, v[156:157]
	global_load_lds_dwordx4 v[10:11], off
	v_lshl_add_u64 v[10:11], s[36:37], 0, v[150:151]
	s_add_i32 m0, s51, 0x1e000
	v_lshlrev_b32_e32 v13, 2, v0
	global_load_lds_dwordx4 v[10:11], off
	v_and_b32_e32 v10, 15, v0
	v_lshlrev_b32_e32 v11, 4, v22
	v_lshl_or_b32 v12, v10, 6, v11
	v_and_b32_e32 v13, 32, v13
	s_cmpk_lt_u32 s20, 0x100
	v_bitop3_b32 v12, v12, s1, v13 bitop3:0xde
	v_lshlrev_b32_e32 v14, 6, v0
	s_movk_i32 s1, 0x3c0
	s_cselect_b64 s[20:21], -1, 0
	s_add_u32 s58, s18, s4
	v_and_or_b32 v14, v14, s1, v11
	s_addc_u32 s59, s22, s5
	s_add_i32 s4, 0, 0x20800
	v_bitop3_b32 v163, s13, v14, v13 bitop3:0xf6
	v_lshrrev_b32_e32 v13, 6, v0
	s_movk_i32 s5, 0x900
	v_mov_b32_e32 v16, s4
	v_and_b32_e32 v14, 7, v0
	s_movk_i32 s1, 0x90
	v_mad_u32_u24 v13, v13, s5, v16
	v_lshl_or_b32 v164, v14, 3, s50
	v_mad_u32_u24 v10, v10, s1, v13
	v_lshl_add_u32 v13, v14, 4, v13
	v_lshlrev_b32_e32 v14, 8, v0
	v_and_b32_e32 v14, 0x18000, v14
	v_lshlrev_b32_e32 v16, 11, v21
	v_or3_b32 v14, v19, v14, v16
	v_add_u32_e32 v14, v14, v20
	v_or_b32_e32 v158, 0x40000, v14
	v_lshlrev_b32_e32 v14, 4, v18
	v_and_b32_e32 v14, 0x38000, v14
	s_waitcnt vmcnt(6)
	v_bfe_u32 v165, v0, 3, 3
	v_or3_b32 v14, v19, v14, v16
	v_mul_u32_u24_e32 v15, 0x90, v165
	v_add_u32_e32 v14, v14, v20
	v_mov_b32_e32 v155, v157
	v_mov_b32_e32 v149, v157
	s_mov_b32 s19, 0
	v_or_b32_e32 v166, 8, v165
	v_mov_b32_e32 v159, v157
	v_or_b32_e32 v160, 0x40000, v14
	v_mov_b32_e32 v161, v157
	s_mov_b32 s22, 0x42800000
	s_add_i32 s60, 0, 0x10000
	s_add_i32 s61, 0, 0x14000
	v_add_u32_e32 v167, 0, v12
	v_lshlrev_b32_e32 v168, 2, v23
	s_mov_b32 s24, 0x3c800000
	v_add_u32_e32 v169, v10, v11
	v_add_u32_e32 v171, v13, v15
	s_mov_b32 s62, 0
	s_barrier
	s_branch .LBB0_1125

; #define PG8_STAGE(bufoff, gbase, voff) do { _Pragma("unroll") for (int _i = 0; _i < 2; ++_i) \
;         __builtin_amdgcn_global_load_lds((const unsigned*)((const char*)(gbase) + (voff)[_i]), (LAS unsigned*)(lds + (bufoff) + ldsw + _i * 8192), 16, 0, 0); } while (0)
; #define PG8_LDA(dst, b, h) do { _Pragma("unroll") for (int m = 0; m < 4; ++m) { if constexpr (F8) dst##8[m] = PG8_LD32(lds + PG8_SA(b, h) + aoff + m * 2048); \
;         else { _Pragma("unroll") for (int k = 0; k < 2; ++k) dst[m][k] = *(const LAS bf16x8*)(lds + PG8_SA(b, h) + aoff + m * 2048 + k * 1024); } } } while (0)
; #define PG8_LDB(dst, b, h) do { _Pragma("unroll") for (int n = 0; n < 2; ++n) { if constexpr (F8) dst##8[n] = PG8_LD32(lds + PG8_SB(b, h) + boff + n * 2048); \
;         else { _Pragma("unroll") for (int k = 0; k < 2; ++k) dst[n][k] = *(const LAS bf16x8*)(lds + PG8_SB(b, h) + boff + n * 2048 + k * 1024); } } } while (0)
; #define PG8_WAIT_V(n) asm volatile("s_waitcnt vmcnt(" #n ")" ::: "memory")
; template <class Epi, class Sched, bool GATHER, bool F8 = false>
; __device__ __forceinline__ void gemm_phase(LAS unsigned char* lds, const int K, const Sched& S, const Epi& E) {
;     ...
;         const bool has_next = S.next(ui + 1, nxt);
;         const char* nA = has_next ? nxt.A : cA; const char* nB = has_next ? nxt.B : cB;
;         for (int t = 0; t < nt; t += 2) {
;             const bool last = (t == nt - 2);
;             const char* a1 = cA + (size_t)(t + 1) * kstep;
;             const char* a2 = last ? nA : cA + (size_t)(t + 2) * kstep; const char* b2 = last ? nB : cB + (size_t)(t + 2) * kstep;
;             const char* a3 = a2 + kstep; const char* b3 = b2 + kstep;
;             if constexpr (GATHER) { if (last && has_next) S.offsets(ui + 1, RA, CA, vN); }
;             PG8_LDB(B0, 0, 0); PG8_LDB(B1, 0, 1); PG8_SCHED; PG8_LDA(At, 0, 0); PG8_STAGE(PG8_SA(1, 1), a1, vA[1]);
;             PG8_WAIT_V(8); PG8_WAIT_L(0); PG8_BAR; PG8_MMA(0, 0, At, B0); PG8_MMA(0, 1, At, B1); PG8_BAR; PG8_SCHED;
;     __device__ __forceinline__ void init(f32x4 (&acc)[2][2][4][2], const Pre& p) const {
; #pragma unroll
;         for (int ai = 0; ai < 2; ++ai)
; #pragma unroll
;             for (int bj = 0; bj < 2; ++bj)
; #pragma unroll
;                 for (int m = 0; m < 4; ++m)
; #pragma unroll
;                     for (int n = 0; n < 2; ++n) acc[ai][bj][m][n] = p.bv[bj][n] * WSCALE;
;     }
.LBB0_1127:
	s_add_u32 s44, s44, 0x80
	s_waitcnt vmcnt(0)
	v_pk_mul_f32 v[20:21], v[80:81], s[22:23] op_sel_hi:[1,0]
	v_pk_mul_f32 v[24:25], v[76:77], s[22:23] op_sel_hi:[1,0]
	v_pk_mul_f32 v[12:13], v[8:9], s[22:23] op_sel_hi:[1,0]
	v_pk_mul_f32 v[16:17], v[4:5], s[22:23] op_sel_hi:[1,0]
	s_addc_u32 s45, s45, 0
	v_pk_mul_f32 v[18:19], v[78:79], s[22:23] op_sel_hi:[1,0]
	v_pk_mul_f32 v[22:23], v[74:75], s[22:23] op_sel_hi:[1,0]
	v_pk_mul_f32 v[10:11], v[6:7], s[22:23] op_sel_hi:[1,0]
	v_pk_mul_f32 v[14:15], v[2:3], s[22:23] op_sel_hi:[1,0]
	s_add_u32 s1, s46, 0x2000
	v_mov_b64_e32 v[28:29], v[16:17]
	v_mov_b64_e32 v[32:33], v[12:13]
	v_mov_b64_e32 v[44:45], v[16:17]
	v_mov_b64_e32 v[48:49], v[12:13]
	v_mov_b64_e32 v[60:61], v[16:17]
	v_mov_b64_e32 v[64:65], v[12:13]
	v_mov_b64_e32 v[36:37], v[24:25]
	v_mov_b64_e32 v[40:41], v[20:21]
	v_mov_b64_e32 v[52:53], v[24:25]
	v_mov_b64_e32 v[56:57], v[20:21]
	v_mov_b64_e32 v[68:69], v[24:25]
	v_mov_b64_e32 v[72:73], v[20:21]
	v_mov_b64_e32 v[84:85], v[16:17]
	v_mov_b64_e32 v[88:89], v[12:13]
	v_mov_b64_e32 v[100:101], v[16:17]
	v_mov_b64_e32 v[104:105], v[12:13]
	v_mov_b64_e32 v[116:117], v[16:17]
	v_mov_b64_e32 v[120:121], v[12:13]
	v_mov_b64_e32 v[132:133], v[16:17]
	v_mov_b64_e32 v[136:137], v[12:13]
	v_mov_b64_e32 v[92:93], v[24:25]
	v_mov_b64_e32 v[96:97], v[20:21]
	v_mov_b64_e32 v[108:109], v[24:25]
	v_mov_b64_e32 v[112:113], v[20:21]
	v_mov_b64_e32 v[124:125], v[24:25]
	v_mov_b64_e32 v[128:129], v[20:21]
	v_mov_b64_e32 v[140:141], v[24:25]
	v_mov_b64_e32 v[144:145], v[20:21]
	s_addc_u32 s13, s47, 0
	s_mov_b32 s18, -2
	v_mov_b64_e32 v[26:27], v[14:15]
	v_mov_b64_e32 v[30:31], v[10:11]
	v_mov_b64_e32 v[42:43], v[14:15]
	v_mov_b64_e32 v[46:47], v[10:11]
	v_mov_b64_e32 v[58:59], v[14:15]
	v_mov_b64_e32 v[62:63], v[10:11]
	v_mov_b64_e32 v[34:35], v[22:23]
	v_mov_b64_e32 v[38:39], v[18:19]
	v_mov_b64_e32 v[50:51], v[22:23]
	v_mov_b64_e32 v[54:55], v[18:19]
	v_mov_b64_e32 v[66:67], v[22:23]
	v_mov_b64_e32 v[70:71], v[18:19]
	v_mov_b64_e32 v[82:83], v[14:15]
	v_mov_b64_e32 v[86:87], v[10:11]
	v_mov_b64_e32 v[98:99], v[14:15]
	v_mov_b64_e32 v[102:103], v[10:11]
	v_mov_b64_e32 v[114:115], v[14:15]
	v_mov_b64_e32 v[118:119], v[10:11]
	v_mov_b64_e32 v[130:131], v[14:15]
	v_mov_b64_e32 v[134:135], v[10:11]
	v_mov_b64_e32 v[90:91], v[22:23]
	v_mov_b64_e32 v[94:95], v[18:19]
	v_mov_b64_e32 v[106:107], v[22:23]
	v_mov_b64_e32 v[110:111], v[18:19]
	v_mov_b64_e32 v[122:123], v[22:23]
	v_mov_b64_e32 v[126:127], v[18:19]
	v_mov_b64_e32 v[138:139], v[22:23]
	v_mov_b64_e32 v[142:143], v[18:19]
.LBB0_1128:
	v_add_u32_e32 v74, s60, v163
	ds_read_b128 v[2:5], v74
	ds_read_b128 v[6:9], v74 offset:1024
	ds_read_b128 v[172:175], v74 offset:2048
	ds_read_b128 v[176:179], v74 offset:3072
	v_add_u32_e32 v74, s61, v163
	ds_read_b128 v[180:183], v74
	ds_read_b128 v[184:187], v74 offset:1024
	ds_read_b128 v[188:191], v74 offset:2048
	ds_read_b128 v[192:195], v74 offset:3072
	s_add_u32 s46, s44, 0x80
	s_addc_u32 s47, s45, 0
	s_cmp_eq_u32 s18, 12
	s_cselect_b32 s49, s41, s47
	s_cselect_b32 s48, s40, s46
	s_cselect_b32 s47, s43, s13
	s_cselect_b32 s46, s42, s1
	v_lshl_add_u64 v[220:221], s[44:45], 0, v[158:159]
	s_add_i32 m0, s51, 0xc000
	ds_read_b128 v[74:77], v167
	ds_read_b128 v[78:81], v167 offset:1024
	ds_read_b128 v[196:199], v167 offset:2048
	ds_read_b128 v[200:203], v167 offset:3072
	ds_read_b128 v[204:207], v167 offset:4096
	ds_read_b128 v[208:211], v167 offset:5120
	ds_read_b128 v[212:215], v167 offset:6144
	ds_read_b128 v[216:219], v167 offset:7168
	global_load_lds_dwordx4 v[220:221], off
	v_lshl_add_u64 v[220:221], s[44:45], 0, v[160:161]
	s_add_i32 m0, s51, 0xe000
	s_nop 0
	global_load_lds_dwordx4 v[220:221], off
	s_waitcnt vmcnt(8)
	s_waitcnt lgkmcnt(0)
	s_barrier
	s_setprio 1
	s_waitcnt lgkmcnt(0)
	v_mfma_scale_f32_16x16x128_f8f6f4 v[142:145], v[2:9], v[74:81], v[142:145], v162, v162 op_sel_hi:[0,0,0]
	v_mfma_scale_f32_16x16x128_f8f6f4 v[138:141], v[172:179], v[74:81], v[138:141], v162, v162 op_sel_hi:[0,0,0]
	v_mfma_scale_f32_16x16x128_f8f6f4 v[126:129], v[2:9], v[196:203], v[126:129], v162, v162 op_sel_hi:[0,0,0]
	v_mfma_scale_f32_16x16x128_f8f6f4 v[122:125], v[172:179], v[196:203], v[122:125], v162, v162 op_sel_hi:[0,0,0]
	v_mfma_scale_f32_16x16x128_f8f6f4 v[110:113], v[2:9], v[204:211], v[110:113], v162, v162 op_sel_hi:[0,0,0]
	v_mfma_scale_f32_16x16x128_f8f6f4 v[106:109], v[172:179], v[204:211], v[106:109], v162, v162 op_sel_hi:[0,0,0]
	v_mfma_scale_f32_16x16x128_f8f6f4 v[94:97], v[2:9], v[212:219], v[94:97], v162, v162 op_sel_hi:[0,0,0]
	v_mfma_scale_f32_16x16x128_f8f6f4 v[90:93], v[172:179], v[212:219], v[90:93], v162, v162 op_sel_hi:[0,0,0]
	s_setprio 0
	s_setprio 1
	v_mfma_scale_f32_16x16x128_f8f6f4 v[134:137], v[180:187], v[74:81], v[134:137], v162, v162 op_sel_hi:[0,0,0]
	v_mfma_scale_f32_16x16x128_f8f6f4 v[130:133], v[188:195], v[74:81], v[130:133], v162, v162 op_sel_hi:[0,0,0]
	v_mfma_scale_f32_16x16x128_f8f6f4 v[118:121], v[180:187], v[196:203], v[118:121], v162, v162 op_sel_hi:[0,0,0]
	v_mfma_scale_f32_16x16x128_f8f6f4 v[114:117], v[188:195], v[196:203], v[114:117], v162, v162 op_sel_hi:[0,0,0]
	v_mfma_scale_f32_16x16x128_f8f6f4 v[102:105], v[180:187], v[204:211], v[102:105], v162, v162 op_sel_hi:[0,0,0]
	v_mfma_scale_f32_16x16x128_f8f6f4 v[98:101], v[188:195], v[204:211], v[98:101], v162, v162 op_sel_hi:[0,0,0]
	v_mfma_scale_f32_16x16x128_f8f6f4 v[86:89], v[180:187], v[212:219], v[86:89], v162, v162 op_sel_hi:[0,0,0]
	v_mfma_scale_f32_16x16x128_f8f6f4 v[82:85], v[188:195], v[212:219], v[82:85], v162, v162 op_sel_hi:[0,0,0]
	s_setprio 0
	s_barrier
; #define PG8_STAGE(bufoff, gbase, voff) do { _Pragma("unroll") for (int _i = 0; _i < 2; ++_i) \
;         __builtin_amdgcn_global_load_lds((const unsigned*)((const char*)(gbase) + (voff)[_i]), (LAS unsigned*)(lds + (bufoff) + ldsw + _i * 8192), 16, 0, 0); } while (0)
; #define PG8_LDA(dst, b, h) do { _Pragma("unroll") for (int m = 0; m < 4; ++m) { if constexpr (F8) dst##8[m] = PG8_LD32(lds + PG8_SA(b, h) + aoff + m * 2048); \
;         else { _Pragma("unroll") for (int k = 0; k < 2; ++k) dst[m][k] = *(const LAS bf16x8*)(lds + PG8_SA(b, h) + aoff + m * 2048 + k * 1024); } } } while (0)
; #define PG8_LDB(dst, b, h) do { _Pragma("unroll") for (int n = 0; n < 2; ++n) { if constexpr (F8) dst##8[n] = PG8_LD32(lds + PG8_SB(b, h) + boff + n * 2048); \
;         else { _Pragma("unroll") for (int k = 0; k < 2; ++k) dst[n][k] = *(const LAS bf16x8*)(lds + PG8_SB(b, h) + boff + n * 2048 + k * 1024); } } } while (0)
; #define PG8_WAIT_V(n) asm volatile("s_waitcnt vmcnt(" #n ")" ::: "memory")
; #define PG8_WAIT_L(n) asm volatile("s_waitcnt lgkmcnt(" #n ")" ::: "memory")
; #define PG8_BAR __builtin_amdgcn_s_barrier()
; #define PG8_SCHED __builtin_amdgcn_sched_barrier(0)
; template <class Epi, class Sched, bool GATHER, bool F8 = false>
; __device__ __forceinline__ void gemm_phase(LAS unsigned char* lds, const int K, const Sched& S, const Epi& E) {
;     ...
;             PG8_LDA(At, 0, 1); PG8_STAGE(PG8_SB(0, 0), b2, voffB); PG8_STAGE(PG8_SB(0, 1), b2 + hstepB, voffB); PG8_STAGE(PG8_SA(0, 0), a2, vN[0]);
;             PG8_WAIT_V(8); PG8_WAIT_L(0); PG8_BAR; PG8_MMA(1, 0, At, B0); PG8_MMA(1, 1, At, B1); PG8_BAR; PG8_SCHED;
;             PG8_LDB(B0, 1, 0); PG8_LDB(B1, 1, 1); PG8_SCHED; PG8_LDA(At, 1, 0); PG8_STAGE(PG8_SA(0, 1), a2, vN[1]);
;             PG8_WAIT_V(8); PG8_WAIT_L(0); PG8_BAR; PG8_MMA(0, 0, At, B0); PG8_MMA(0, 1, At, B1); PG8_BAR; PG8_SCHED;
	s_add_i32 s65, s60, s25
	v_lshl_add_u64 v[74:75], s[46:47], 0, v[156:157]
	s_mov_b32 m0, s65
	ds_read_b128 v[196:199], v167 offset:16384
	ds_read_b128 v[200:203], v167 offset:17408
	ds_read_b128 v[204:207], v167 offset:18432
	ds_read_b128 v[208:211], v167 offset:19456
	ds_read_b128 v[212:215], v167 offset:20480
	ds_read_b128 v[216:219], v167 offset:21504
	ds_read_b128 v[220:223], v167 offset:22528
	ds_read_b128 v[224:227], v167 offset:23552
	global_load_lds_dwordx4 v[74:75], off
	s_add_i32 m0, s65, 0x2000
	s_add_u32 s66, s46, 0x10000
	v_lshl_add_u64 v[76:77], s[46:47], 0, v[150:151]
	s_addc_u32 s67, s47, 0
	s_add_i32 s65, s61, s25
	global_load_lds_dwordx4 v[76:77], off
	v_lshl_add_u64 v[78:79], s[66:67], 0, v[156:157]
	s_mov_b32 m0, s65
	v_lshl_add_u64 v[80:81], s[48:49], 0, v[146:147]
	global_load_lds_dwordx4 v[78:79], off
	v_lshl_add_u64 v[78:79], s[66:67], 0, v[150:151]
	s_add_i32 m0, s65, 0x2000
	s_nop 0
	global_load_lds_dwordx4 v[78:79], off
	v_lshl_add_u64 v[78:79], s[48:49], 0, v[152:153]
	s_mov_b32 m0, s51
	s_nop 0
	global_load_lds_dwordx4 v[78:79], off
	s_mov_b32 m0, s52
	s_nop 0
	global_load_lds_dwordx4 v[80:81], off
	s_waitcnt vmcnt(8)
	s_waitcnt lgkmcnt(0)
	s_barrier
	s_setprio 1
	s_waitcnt lgkmcnt(0)
	v_mfma_scale_f32_16x16x128_f8f6f4 v[70:73], v[2:9], v[196:203], v[70:73], v162, v162 op_sel_hi:[0,0,0]
	v_mfma_scale_f32_16x16x128_f8f6f4 v[66:69], v[172:179], v[196:203], v[66:69], v162, v162 op_sel_hi:[0,0,0]
	v_mfma_scale_f32_16x16x128_f8f6f4 v[54:57], v[2:9], v[204:211], v[54:57], v162, v162 op_sel_hi:[0,0,0]
	v_mfma_scale_f32_16x16x128_f8f6f4 v[50:53], v[172:179], v[204:211], v[50:53], v162, v162 op_sel_hi:[0,0,0]
	v_mfma_scale_f32_16x16x128_f8f6f4 v[38:41], v[2:9], v[212:219], v[38:41], v162, v162 op_sel_hi:[0,0,0]
	v_mfma_scale_f32_16x16x128_f8f6f4 v[34:37], v[172:179], v[212:219], v[34:37], v162, v162 op_sel_hi:[0,0,0]
	v_mfma_scale_f32_16x16x128_f8f6f4 v[18:21], v[2:9], v[220:227], v[18:21], v162, v162 op_sel_hi:[0,0,0]
	v_mfma_scale_f32_16x16x128_f8f6f4 v[22:25], v[172:179], v[220:227], v[22:25], v162, v162 op_sel_hi:[0,0,0]
	s_setprio 0
	s_setprio 1
	v_mfma_scale_f32_16x16x128_f8f6f4 v[62:65], v[180:187], v[196:203], v[62:65], v162, v162 op_sel_hi:[0,0,0]
	v_mfma_scale_f32_16x16x128_f8f6f4 v[58:61], v[188:195], v[196:203], v[58:61], v162, v162 op_sel_hi:[0,0,0]
	v_mfma_scale_f32_16x16x128_f8f6f4 v[46:49], v[180:187], v[204:211], v[46:49], v162, v162 op_sel_hi:[0,0,0]
	v_mfma_scale_f32_16x16x128_f8f6f4 v[42:45], v[188:195], v[204:211], v[42:45], v162, v162 op_sel_hi:[0,0,0]
	v_mfma_scale_f32_16x16x128_f8f6f4 v[30:33], v[180:187], v[212:219], v[30:33], v162, v162 op_sel_hi:[0,0,0]
	v_mfma_scale_f32_16x16x128_f8f6f4 v[26:29], v[188:195], v[212:219], v[26:29], v162, v162 op_sel_hi:[0,0,0]
	v_mfma_scale_f32_16x16x128_f8f6f4 v[10:13], v[180:187], v[220:227], v[10:13], v162, v162 op_sel_hi:[0,0,0]
	v_mfma_scale_f32_16x16x128_f8f6f4 v[14:17], v[188:195], v[220:227], v[14:17], v162, v162 op_sel_hi:[0,0,0]
	s_setprio 0
	s_barrier
	s_add_i32 s65, 0, 0x18000
	s_add_i32 s66, 0, 0x1c000
	v_add_u32_e32 v2, s65, v163
	v_add_u32_e32 v192, s66, v163
	ds_read_b128 v[172:175], v2
	ds_read_b128 v[176:179], v2 offset:1024
	ds_read_b128 v[180:183], v2 offset:2048
	ds_read_b128 v[184:187], v2 offset:3072
	ds_read_b128 v[2:5], v192
	ds_read_b128 v[6:9], v192 offset:1024
	ds_read_b128 v[188:191], v192 offset:2048
	ds_read_b128 v[192:195], v192 offset:3072
	s_mov_b32 m0, s53
	v_lshl_add_u64 v[228:229], s[48:49], 0, v[154:155]
	ds_read_b128 v[196:199], v167 offset:32768
	ds_read_b128 v[200:203], v167 offset:33792
	ds_read_b128 v[204:207], v167 offset:34816
	ds_read_b128 v[208:211], v167 offset:35840
	ds_read_b128 v[212:215], v167 offset:36864
	ds_read_b128 v[216:219], v167 offset:37888
	ds_read_b128 v[220:223], v167 offset:38912
	ds_read_b128 v[224:227], v167 offset:39936
	global_load_lds_dwordx4 v[228:229], off
	v_lshl_add_u64 v[228:229], s[48:49], 0, v[148:149]
	s_mov_b32 m0, s54
	s_nop 0
	global_load_lds_dwordx4 v[228:229], off
	s_waitcnt vmcnt(8)
	s_waitcnt lgkmcnt(0)
	s_barrier
; #define PG8_STAGE(bufoff, gbase, voff) do { _Pragma("unroll") for (int _i = 0; _i < 2; ++_i) \
;         __builtin_amdgcn_global_load_lds((const unsigned*)((const char*)(gbase) + (voff)[_i]), (LAS unsigned*)(lds + (bufoff) + ldsw + _i * 8192), 16, 0, 0); } while (0)
; #define PG8_LDA(dst, b, h) do { _Pragma("unroll") for (int m = 0; m < 4; ++m) { if constexpr (F8) dst##8[m] = PG8_LD32(lds + PG8_SA(b, h) + aoff + m * 2048); \
;         else { _Pragma("unroll") for (int k = 0; k < 2; ++k) dst[m][k] = *(const LAS bf16x8*)(lds + PG8_SA(b, h) + aoff + m * 2048 + k * 1024); } } } while (0)
; #define PG8_WAIT_V(n) asm volatile("s_waitcnt vmcnt(" #n ")" ::: "memory")
; #define PG8_WAIT_L(n) asm volatile("s_waitcnt lgkmcnt(" #n ")" ::: "memory")
; #define PG8_BAR __builtin_amdgcn_s_barrier()
; #define PG8_SCHED __builtin_amdgcn_sched_barrier(0)
; template <class Epi, class Sched, bool GATHER, bool F8 = false>
; __device__ __forceinline__ void gemm_phase(LAS unsigned char* lds, const int K, const Sched& S, const Epi& E) {
;     ...
;             PG8_WAIT_V(8); PG8_WAIT_L(0); PG8_BAR; PG8_MMA(0, 0, At, B0); PG8_MMA(0, 1, At, B1); PG8_BAR; PG8_SCHED;
;             PG8_LDA(At, 1, 1); PG8_STAGE(PG8_SB(1, 0), b3, voffB); PG8_STAGE(PG8_SB(1, 1), b3 + hstepB, voffB); PG8_STAGE(PG8_SA(1, 0), a3, vN[0]);
;             PG8_WAIT_V(8); PG8_WAIT_L(0); PG8_BAR; PG8_MMA(1, 0, At, B0); PG8_MMA(1, 1, At, B1); PG8_BAR; PG8_SCHED;
;         }
	s_setprio 1
	s_waitcnt lgkmcnt(0)
	v_mfma_scale_f32_16x16x128_f8f6f4 v[142:145], v[172:179], v[196:203], v[142:145], v162, v162 op_sel_hi:[0,0,0]
	v_mfma_scale_f32_16x16x128_f8f6f4 v[138:141], v[180:187], v[196:203], v[138:141], v162, v162 op_sel_hi:[0,0,0]
	v_mfma_scale_f32_16x16x128_f8f6f4 v[126:129], v[172:179], v[204:211], v[126:129], v162, v162 op_sel_hi:[0,0,0]
	v_mfma_scale_f32_16x16x128_f8f6f4 v[122:125], v[180:187], v[204:211], v[122:125], v162, v162 op_sel_hi:[0,0,0]
	v_mfma_scale_f32_16x16x128_f8f6f4 v[110:113], v[172:179], v[212:219], v[110:113], v162, v162 op_sel_hi:[0,0,0]
	v_mfma_scale_f32_16x16x128_f8f6f4 v[106:109], v[180:187], v[212:219], v[106:109], v162, v162 op_sel_hi:[0,0,0]
	v_mfma_scale_f32_16x16x128_f8f6f4 v[94:97], v[172:179], v[220:227], v[94:97], v162, v162 op_sel_hi:[0,0,0]
	v_mfma_scale_f32_16x16x128_f8f6f4 v[90:93], v[180:187], v[220:227], v[90:93], v162, v162 op_sel_hi:[0,0,0]
	s_setprio 0
	s_setprio 1
	v_mfma_scale_f32_16x16x128_f8f6f4 v[134:137], v[2:9], v[196:203], v[134:137], v162, v162 op_sel_hi:[0,0,0]
	v_mfma_scale_f32_16x16x128_f8f6f4 v[130:133], v[188:195], v[196:203], v[130:133], v162, v162 op_sel_hi:[0,0,0]
	v_mfma_scale_f32_16x16x128_f8f6f4 v[118:121], v[2:9], v[204:211], v[118:121], v162, v162 op_sel_hi:[0,0,0]
	v_mfma_scale_f32_16x16x128_f8f6f4 v[114:117], v[188:195], v[204:211], v[114:117], v162, v162 op_sel_hi:[0,0,0]
	v_mfma_scale_f32_16x16x128_f8f6f4 v[102:105], v[2:9], v[212:219], v[102:105], v162, v162 op_sel_hi:[0,0,0]
	v_mfma_scale_f32_16x16x128_f8f6f4 v[98:101], v[188:195], v[212:219], v[98:101], v162, v162 op_sel_hi:[0,0,0]
	v_mfma_scale_f32_16x16x128_f8f6f4 v[86:89], v[2:9], v[220:227], v[86:89], v162, v162 op_sel_hi:[0,0,0]
	v_mfma_scale_f32_16x16x128_f8f6f4 v[82:85], v[188:195], v[220:227], v[82:85], v162, v162 op_sel_hi:[0,0,0]
	s_setprio 0
	s_barrier
	s_add_i32 s48, s65, s25
	v_lshl_add_u64 v[74:75], v[74:75], 0, s[100:101]
	s_mov_b32 m0, s48
	ds_read_b128 v[196:199], v167 offset:49152
	ds_read_b128 v[200:203], v167 offset:50176
	ds_read_b128 v[204:207], v167 offset:51200
	ds_read_b128 v[208:211], v167 offset:52224
	ds_read_b128 v[212:215], v167 offset:53248
	ds_read_b128 v[216:219], v167 offset:54272
	ds_read_b128 v[220:223], v167 offset:55296
	ds_read_b128 v[224:227], v167 offset:56320
	global_load_lds_dwordx4 v[74:75], off
	s_add_i32 m0, s48, 0x2000
	s_add_u32 s46, s46, 0x11000
	v_lshl_add_u64 v[74:75], v[76:77], 0, s[100:101]
	s_addc_u32 s47, s47, 0
	s_add_i32 s48, s66, s25
	global_load_lds_dwordx4 v[74:75], off
	v_lshl_add_u64 v[74:75], s[46:47], 0, v[156:157]
	s_mov_b32 m0, s48
	s_nop 0
	global_load_lds_dwordx4 v[74:75], off
	v_lshl_add_u64 v[74:75], s[46:47], 0, v[150:151]
	s_add_i32 m0, s48, 0x2000
	s_nop 0
	global_load_lds_dwordx4 v[74:75], off
	v_lshl_add_u64 v[74:75], v[78:79], 0, s[16:17]
	s_mov_b32 m0, s56
	s_nop 0
	global_load_lds_dwordx4 v[74:75], off
	v_lshl_add_u64 v[74:75], v[80:81], 0, s[16:17]
	s_mov_b32 m0, s57
	s_nop 0
	global_load_lds_dwordx4 v[74:75], off
	s_waitcnt vmcnt(8)
	s_waitcnt lgkmcnt(0)
	s_barrier
	s_setprio 1
	s_waitcnt lgkmcnt(0)
	v_mfma_scale_f32_16x16x128_f8f6f4 v[70:73], v[172:179], v[196:203], v[70:73], v162, v162 op_sel_hi:[0,0,0]
	v_mfma_scale_f32_16x16x128_f8f6f4 v[66:69], v[180:187], v[196:203], v[66:69], v162, v162 op_sel_hi:[0,0,0]
	v_mfma_scale_f32_16x16x128_f8f6f4 v[54:57], v[172:179], v[204:211], v[54:57], v162, v162 op_sel_hi:[0,0,0]
	v_mfma_scale_f32_16x16x128_f8f6f4 v[50:53], v[180:187], v[204:211], v[50:53], v162, v162 op_sel_hi:[0,0,0]
	v_mfma_scale_f32_16x16x128_f8f6f4 v[38:41], v[172:179], v[212:219], v[38:41], v162, v162 op_sel_hi:[0,0,0]
	v_mfma_scale_f32_16x16x128_f8f6f4 v[34:37], v[180:187], v[212:219], v[34:37], v162, v162 op_sel_hi:[0,0,0]
	v_mfma_scale_f32_16x16x128_f8f6f4 v[18:21], v[172:179], v[220:227], v[18:21], v162, v162 op_sel_hi:[0,0,0]
	v_mfma_scale_f32_16x16x128_f8f6f4 v[22:25], v[180:187], v[220:227], v[22:25], v162, v162 op_sel_hi:[0,0,0]
	s_setprio 0
	s_setprio 1
	v_mfma_scale_f32_16x16x128_f8f6f4 v[62:65], v[2:9], v[196:203], v[62:65], v162, v162 op_sel_hi:[0,0,0]
	v_mfma_scale_f32_16x16x128_f8f6f4 v[58:61], v[188:195], v[196:203], v[58:61], v162, v162 op_sel_hi:[0,0,0]
	v_mfma_scale_f32_16x16x128_f8f6f4 v[46:49], v[2:9], v[204:211], v[46:49], v162, v162 op_sel_hi:[0,0,0]
	v_mfma_scale_f32_16x16x128_f8f6f4 v[42:45], v[188:195], v[204:211], v[42:45], v162, v162 op_sel_hi:[0,0,0]
	v_mfma_scale_f32_16x16x128_f8f6f4 v[30:33], v[2:9], v[212:219], v[30:33], v162, v162 op_sel_hi:[0,0,0]
	v_mfma_scale_f32_16x16x128_f8f6f4 v[26:29], v[188:195], v[212:219], v[26:29], v162, v162 op_sel_hi:[0,0,0]
	v_mfma_scale_f32_16x16x128_f8f6f4 v[10:13], v[2:9], v[220:227], v[10:13], v162, v162 op_sel_hi:[0,0,0]
	v_mfma_scale_f32_16x16x128_f8f6f4 v[14:17], v[188:195], v[220:227], v[14:17], v162, v162 op_sel_hi:[0,0,0]
	s_setprio 0
	s_barrier
	s_add_i32 s18, s18, 2
	s_add_u32 s44, s44, 0x100
	s_addc_u32 s45, s45, 0
	s_add_u32 s1, s1, 0x2000
	s_addc_u32 s13, s13, 0
	s_cmp_gt_u32 s18, 13
	s_cbranch_scc0 .LBB0_1128
	s_and_b64 vcc, exec, s[20:21]
	s_cbranch_vccz .LBB0_1131
	s_barrier
